# fp8 GEMM K-loops without the per-segment s_setprio toggles (both halves at priority 0)
# baseline (speedup 1.0000x reference)
.LBB0_258:
	s_lshl_b64 s[2:3], s[82:83], 7
	s_add_u32 s26, s4, s2
	v_mov_b32_e32 v2, v184
	v_readfirstlane_b32 s28, v187
	ds_read_b128 v[218:221], v214 offset:16384
	ds_read_b128 v[222:225], v214 offset:17408
	ds_read_b128 v[226:229], v215 offset:16384
	ds_read_b128 v[230:233], v215 offset:17408
	ds_read_b128 v[234:237], v216 offset:16384
	ds_read_b128 v[238:241], v216 offset:17408
	ds_read_b128 v[242:245], v217 offset:16384
	ds_read_b128 v[246:249], v217 offset:17408
	s_addc_u32 s27, s5, s3
	s_mov_b32 m0, s28
	s_add_u32 s28, s26, 0x10000
	global_load_lds_dwordx4 v2, s[26:27]
	v_mov_b32_e32 v2, v184
	v_readfirstlane_b32 s30, v188
	s_addc_u32 s29, s27, 0
	s_mov_b32 m0, s30
	v_readfirstlane_b32 s30, v189
	global_load_lds_dwordx4 v2, s[28:29]
	s_add_u32 s28, s26, 0x20000
	v_mov_b32_e32 v2, v184
	s_addc_u32 s29, s27, 0
	s_mov_b32 m0, s30
	s_add_u32 s26, s26, 0x30000
	global_load_lds_dwordx4 v2, s[28:29]
	v_mov_b32_e32 v2, v184
	v_readfirstlane_b32 s28, v190
	s_addc_u32 s27, s27, 0
	s_mov_b32 m0, s28
	s_add_u32 s2, s6, s2
	global_load_lds_dwordx4 v2, s[26:27]
	v_mov_b32_e32 v2, v180
	v_readfirstlane_b32 s26, v191
	s_addc_u32 s3, s7, s3
	s_mov_b32 m0, s26
	v_readfirstlane_b32 s26, v201
	global_load_lds_dwordx4 v2, s[2:3]
	v_mov_b32_e32 v2, v181
	s_mov_b32 m0, s26
	s_nop 0
	global_load_lds_dwordx4 v2, s[2:3]
	s_waitcnt vmcnt(8)
	s_waitcnt lgkmcnt(0)
	s_barrier
	s_waitcnt lgkmcnt(0)
	v_mfma_scale_f32_16x16x128_f8f6f4 v[144:147], v[20:27], v[218:225], v[144:147], v186, v185 op_sel_hi:[0,0,0]
	v_mfma_scale_f32_16x16x128_f8f6f4 v[140:143], v[28:35], v[218:225], v[140:143], v186, v185 op_sel_hi:[0,0,0]
	v_mfma_scale_f32_16x16x128_f8f6f4 v[136:139], v[20:27], v[226:233], v[136:139], v186, v185 op_sel_hi:[0,0,0]
	v_mfma_scale_f32_16x16x128_f8f6f4 v[132:135], v[28:35], v[226:233], v[132:135], v186, v185 op_sel_hi:[0,0,0]
	v_mfma_scale_f32_16x16x128_f8f6f4 v[128:131], v[20:27], v[234:241], v[128:131], v186, v185 op_sel_hi:[0,0,0]
	v_mfma_scale_f32_16x16x128_f8f6f4 v[124:127], v[28:35], v[234:241], v[124:127], v186, v185 op_sel_hi:[0,0,0]
	v_mfma_scale_f32_16x16x128_f8f6f4 v[120:123], v[20:27], v[242:249], v[120:123], v186, v185 op_sel_hi:[0,0,0]
	v_mfma_scale_f32_16x16x128_f8f6f4 v[116:119], v[28:35], v[242:249], v[116:119], v186, v185 op_sel_hi:[0,0,0]
	v_mfma_scale_f32_16x16x128_f8f6f4 v[80:83], v[4:11], v[218:225], v[80:83], v186, v185 op_sel_hi:[0,0,0]
	v_mfma_scale_f32_16x16x128_f8f6f4 v[76:79], v[12:19], v[218:225], v[76:79], v186, v185 op_sel_hi:[0,0,0]
	v_mfma_scale_f32_16x16x128_f8f6f4 v[72:75], v[4:11], v[226:233], v[72:75], v186, v185 op_sel_hi:[0,0,0]
	v_mfma_scale_f32_16x16x128_f8f6f4 v[68:71], v[12:19], v[226:233], v[68:71], v186, v185 op_sel_hi:[0,0,0]
	v_mfma_scale_f32_16x16x128_f8f6f4 v[64:67], v[4:11], v[234:241], v[64:67], v186, v185 op_sel_hi:[0,0,0]
	v_mfma_scale_f32_16x16x128_f8f6f4 v[60:63], v[12:19], v[234:241], v[60:63], v186, v185 op_sel_hi:[0,0,0]
	v_mfma_scale_f32_16x16x128_f8f6f4 v[56:59], v[4:11], v[242:249], v[56:59], v186, v185 op_sel_hi:[0,0,0]
	v_mfma_scale_f32_16x16x128_f8f6f4 v[52:55], v[12:19], v[242:249], v[52:55], v186, v185 op_sel_hi:[0,0,0]
	s_barrier
	ds_read_b128 v[20:23], v212
	ds_read_b128 v[24:27], v212 offset:1024
	ds_read_b128 v[28:31], v212 offset:2048
	ds_read_b128 v[32:35], v212 offset:3072
	ds_read_b128 v[4:7], v213
	ds_read_b128 v[8:11], v213 offset:1024
	ds_read_b128 v[12:15], v213 offset:2048
	ds_read_b128 v[16:19], v213 offset:3072
	v_mov_b32_e32 v2, v182
	v_readfirstlane_b32 s26, v202
	ds_read_b128 v[218:221], v214 offset:32768
	ds_read_b128 v[222:225], v214 offset:33792
	ds_read_b128 v[226:229], v215 offset:32768
	ds_read_b128 v[230:233], v215 offset:33792
	ds_read_b128 v[234:237], v216 offset:32768
	ds_read_b128 v[238:241], v216 offset:33792
	ds_read_b128 v[242:245], v217 offset:32768
	ds_read_b128 v[246:249], v217 offset:33792
	s_mov_b32 m0, s26
	v_readfirstlane_b32 s26, v203
	global_load_lds_dwordx4 v2, s[2:3]
	v_mov_b32_e32 v2, v183
	s_mov_b32 m0, s26
	s_nop 0
	global_load_lds_dwordx4 v2, s[2:3]
	s_waitcnt vmcnt(8)
	s_waitcnt lgkmcnt(0)
	s_barrier
	s_waitcnt lgkmcnt(0)
	v_mfma_scale_f32_16x16x128_f8f6f4 v[176:179], v[20:27], v[218:225], v[176:179], v186, v185 op_sel_hi:[0,0,0]
	v_mfma_scale_f32_16x16x128_f8f6f4 v[172:175], v[28:35], v[218:225], v[172:175], v186, v185 op_sel_hi:[0,0,0]
	v_mfma_scale_f32_16x16x128_f8f6f4 v[168:171], v[20:27], v[226:233], v[168:171], v186, v185 op_sel_hi:[0,0,0]
	v_mfma_scale_f32_16x16x128_f8f6f4 v[164:167], v[28:35], v[226:233], v[164:167], v186, v185 op_sel_hi:[0,0,0]
	v_mfma_scale_f32_16x16x128_f8f6f4 v[160:163], v[20:27], v[234:241], v[160:163], v186, v185 op_sel_hi:[0,0,0]
	v_mfma_scale_f32_16x16x128_f8f6f4 v[156:159], v[28:35], v[234:241], v[156:159], v186, v185 op_sel_hi:[0,0,0]
	v_mfma_scale_f32_16x16x128_f8f6f4 v[152:155], v[20:27], v[242:249], v[152:155], v186, v185 op_sel_hi:[0,0,0]
	v_mfma_scale_f32_16x16x128_f8f6f4 v[148:151], v[28:35], v[242:249], v[148:151], v186, v185 op_sel_hi:[0,0,0]
	v_mfma_scale_f32_16x16x128_f8f6f4 v[112:115], v[4:11], v[218:225], v[112:115], v186, v185 op_sel_hi:[0,0,0]
	v_mfma_scale_f32_16x16x128_f8f6f4 v[108:111], v[12:19], v[218:225], v[108:111], v186, v185 op_sel_hi:[0,0,0]
	v_mfma_scale_f32_16x16x128_f8f6f4 v[104:107], v[4:11], v[226:233], v[104:107], v186, v185 op_sel_hi:[0,0,0]
	v_mfma_scale_f32_16x16x128_f8f6f4 v[100:103], v[12:19], v[226:233], v[100:103], v186, v185 op_sel_hi:[0,0,0]
	v_mfma_scale_f32_16x16x128_f8f6f4 v[96:99], v[4:11], v[234:241], v[96:99], v186, v185 op_sel_hi:[0,0,0]
	v_mfma_scale_f32_16x16x128_f8f6f4 v[92:95], v[12:19], v[234:241], v[92:95], v186, v185 op_sel_hi:[0,0,0]
	v_mfma_scale_f32_16x16x128_f8f6f4 v[88:91], v[4:11], v[242:249], v[88:91], v186, v185 op_sel_hi:[0,0,0]
	v_mfma_scale_f32_16x16x128_f8f6f4 v[84:87], v[12:19], v[242:249], v[84:87], v186, v185 op_sel_hi:[0,0,0]
	s_barrier
	s_add_i32 s82, s82, 1
	s_lshl_b64 s[2:3], s[82:83], 7
	s_add_u32 s26, s4, s2
	v_mov_b32_e32 v2, v184
	v_readfirstlane_b32 s28, v204
	ds_read_b128 v[218:221], v214 offset:49152
	ds_read_b128 v[222:225], v214 offset:50176
	ds_read_b128 v[226:229], v215 offset:49152
	ds_read_b128 v[230:233], v215 offset:50176
	ds_read_b128 v[234:237], v216 offset:49152
	ds_read_b128 v[238:241], v216 offset:50176
	ds_read_b128 v[242:245], v217 offset:49152
	ds_read_b128 v[246:249], v217 offset:50176
	s_addc_u32 s27, s5, s3
	s_mov_b32 m0, s28
	s_add_u32 s28, s26, 0x10000
	global_load_lds_dwordx4 v2, s[26:27]
	v_mov_b32_e32 v2, v184
	v_readfirstlane_b32 s30, v205
	s_addc_u32 s29, s27, 0
	s_mov_b32 m0, s30
	v_readfirstlane_b32 s30, v208
	global_load_lds_dwordx4 v2, s[28:29]
	s_add_u32 s28, s26, 0x20000
	v_mov_b32_e32 v2, v184
	s_addc_u32 s29, s27, 0
	s_mov_b32 m0, s30
	s_add_u32 s26, s26, 0x30000
	global_load_lds_dwordx4 v2, s[28:29]
	v_mov_b32_e32 v2, v184
	v_readfirstlane_b32 s28, v209
	s_addc_u32 s27, s27, 0
	s_mov_b32 m0, s28
	s_add_u32 s2, s6, s2
	global_load_lds_dwordx4 v2, s[26:27]
	v_mov_b32_e32 v2, v180
	v_readfirstlane_b32 s26, v206
	s_addc_u32 s3, s7, s3
	s_mov_b32 m0, s26
	v_readfirstlane_b32 s26, v207
	global_load_lds_dwordx4 v2, s[2:3]
	v_mov_b32_e32 v2, v181
	s_mov_b32 m0, s26
	s_nop 0
	global_load_lds_dwordx4 v2, s[2:3]
	s_waitcnt vmcnt(8)
	s_waitcnt lgkmcnt(0)
	s_barrier
	s_waitcnt lgkmcnt(0)
	v_mfma_scale_f32_16x16x128_f8f6f4 v[144:147], v[20:27], v[218:225], v[144:147], v186, v185 op_sel_hi:[0,0,0]
	v_mfma_scale_f32_16x16x128_f8f6f4 v[140:143], v[28:35], v[218:225], v[140:143], v186, v185 op_sel_hi:[0,0,0]
	v_mfma_scale_f32_16x16x128_f8f6f4 v[136:139], v[20:27], v[226:233], v[136:139], v186, v185 op_sel_hi:[0,0,0]
	v_mfma_scale_f32_16x16x128_f8f6f4 v[132:135], v[28:35], v[226:233], v[132:135], v186, v185 op_sel_hi:[0,0,0]
	v_mfma_scale_f32_16x16x128_f8f6f4 v[128:131], v[20:27], v[234:241], v[128:131], v186, v185 op_sel_hi:[0,0,0]
	v_mfma_scale_f32_16x16x128_f8f6f4 v[124:127], v[28:35], v[234:241], v[124:127], v186, v185 op_sel_hi:[0,0,0]
	v_mfma_scale_f32_16x16x128_f8f6f4 v[120:123], v[20:27], v[242:249], v[120:123], v186, v185 op_sel_hi:[0,0,0]
	v_mfma_scale_f32_16x16x128_f8f6f4 v[116:119], v[28:35], v[242:249], v[116:119], v186, v185 op_sel_hi:[0,0,0]
	v_mfma_scale_f32_16x16x128_f8f6f4 v[80:83], v[4:11], v[218:225], v[80:83], v186, v185 op_sel_hi:[0,0,0]
	v_mfma_scale_f32_16x16x128_f8f6f4 v[76:79], v[12:19], v[218:225], v[76:79], v186, v185 op_sel_hi:[0,0,0]
	v_mfma_scale_f32_16x16x128_f8f6f4 v[72:75], v[4:11], v[226:233], v[72:75], v186, v185 op_sel_hi:[0,0,0]
	v_mfma_scale_f32_16x16x128_f8f6f4 v[68:71], v[12:19], v[226:233], v[68:71], v186, v185 op_sel_hi:[0,0,0]
	v_mfma_scale_f32_16x16x128_f8f6f4 v[64:67], v[4:11], v[234:241], v[64:67], v186, v185 op_sel_hi:[0,0,0]
	v_mfma_scale_f32_16x16x128_f8f6f4 v[60:63], v[12:19], v[234:241], v[60:63], v186, v185 op_sel_hi:[0,0,0]
	v_mfma_scale_f32_16x16x128_f8f6f4 v[56:59], v[4:11], v[242:249], v[56:59], v186, v185 op_sel_hi:[0,0,0]
	v_mfma_scale_f32_16x16x128_f8f6f4 v[52:55], v[12:19], v[242:249], v[52:55], v186, v185 op_sel_hi:[0,0,0]
	s_barrier
	s_add_i32 s25, s25, 2
	s_add_u32 s12, s12, 0x100
	s_addc_u32 s13, s13, 0
	s_cmp_gt_u32 s25, 5
	s_cbranch_scc1 .LBB0_263
.LBB0_259:
	ds_read_b128 v[20:23], v210
	ds_read_b128 v[24:27], v210 offset:1024
	ds_read_b128 v[28:31], v210 offset:2048
	ds_read_b128 v[32:35], v210 offset:3072
	ds_read_b128 v[4:7], v211
	ds_read_b128 v[8:11], v211 offset:1024
	ds_read_b128 v[12:15], v211 offset:2048
	ds_read_b128 v[16:19], v211 offset:3072
	s_add_u32 s2, s6, s12
	s_addc_u32 s3, s7, s13
	v_add_u32_e32 v192, 0xc000, v191
	s_add_u32 s2, s2, 0x80
	v_mov_b32_e32 v2, v182
	v_readfirstlane_b32 s26, v192
	v_add_u32_e32 v192, 0xe000, v191
	ds_read_b128 v[218:221], v214
	ds_read_b128 v[222:225], v214 offset:1024
	ds_read_b128 v[226:229], v215
	ds_read_b128 v[230:233], v215 offset:1024
	ds_read_b128 v[234:237], v216
	ds_read_b128 v[238:241], v216 offset:1024
	ds_read_b128 v[242:245], v217
	ds_read_b128 v[246:249], v217 offset:1024
	s_addc_u32 s3, s3, 0
	s_mov_b32 m0, s26
	v_readfirstlane_b32 s26, v192
	global_load_lds_dwordx4 v2, s[2:3]
	v_mov_b32_e32 v2, v183
	s_mov_b32 m0, s26
	s_nop 0
	global_load_lds_dwordx4 v2, s[2:3]
	s_waitcnt vmcnt(8)
	s_waitcnt lgkmcnt(0)
	s_barrier
	s_waitcnt lgkmcnt(0)
	v_mfma_scale_f32_16x16x128_f8f6f4 v[176:179], v[20:27], v[218:225], v[176:179], v186, v185 op_sel_hi:[0,0,0]
	v_mfma_scale_f32_16x16x128_f8f6f4 v[172:175], v[28:35], v[218:225], v[172:175], v186, v185 op_sel_hi:[0,0,0]
	v_mfma_scale_f32_16x16x128_f8f6f4 v[168:171], v[20:27], v[226:233], v[168:171], v186, v185 op_sel_hi:[0,0,0]
	v_mfma_scale_f32_16x16x128_f8f6f4 v[164:167], v[28:35], v[226:233], v[164:167], v186, v185 op_sel_hi:[0,0,0]
	v_mfma_scale_f32_16x16x128_f8f6f4 v[160:163], v[20:27], v[234:241], v[160:163], v186, v185 op_sel_hi:[0,0,0]
	v_mfma_scale_f32_16x16x128_f8f6f4 v[156:159], v[28:35], v[234:241], v[156:159], v186, v185 op_sel_hi:[0,0,0]
	v_mfma_scale_f32_16x16x128_f8f6f4 v[152:155], v[20:27], v[242:249], v[152:155], v186, v185 op_sel_hi:[0,0,0]
	v_mfma_scale_f32_16x16x128_f8f6f4 v[148:151], v[28:35], v[242:249], v[148:151], v186, v185 op_sel_hi:[0,0,0]
	v_mfma_scale_f32_16x16x128_f8f6f4 v[112:115], v[4:11], v[218:225], v[112:115], v186, v185 op_sel_hi:[0,0,0]
	v_mfma_scale_f32_16x16x128_f8f6f4 v[108:111], v[12:19], v[218:225], v[108:111], v186, v185 op_sel_hi:[0,0,0]
	v_mfma_scale_f32_16x16x128_f8f6f4 v[104:107], v[4:11], v[226:233], v[104:107], v186, v185 op_sel_hi:[0,0,0]
	v_mfma_scale_f32_16x16x128_f8f6f4 v[100:103], v[12:19], v[226:233], v[100:103], v186, v185 op_sel_hi:[0,0,0]
	v_mfma_scale_f32_16x16x128_f8f6f4 v[96:99], v[4:11], v[234:241], v[96:99], v186, v185 op_sel_hi:[0,0,0]
	v_mfma_scale_f32_16x16x128_f8f6f4 v[92:95], v[12:19], v[234:241], v[92:95], v186, v185 op_sel_hi:[0,0,0]
	v_mfma_scale_f32_16x16x128_f8f6f4 v[88:91], v[4:11], v[242:249], v[88:91], v186, v185 op_sel_hi:[0,0,0]
	v_mfma_scale_f32_16x16x128_f8f6f4 v[84:87], v[12:19], v[242:249], v[84:87], v186, v185 op_sel_hi:[0,0,0]
	s_cmp_lg_u32 s25, 4
	s_barrier
	s_cbranch_scc1 .LBB0_262
	s_cmpk_gt_u32 s15, 0xd7f
	s_mov_b64 s[20:21], 0
	s_cbranch_scc1 .LBB0_257
	v_readlane_b32 s2, v255, 41
	v_readlane_b32 s4, v255, 40
	v_mov_b32_e32 v2, v0
	s_mov_b64 s[20:21], -1
	v_ashrrev_i32_e32 v181, 31, v2
	v_lshrrev_b32_e32 v181, 26, v181
	v_lshlrev_b32_e32 v180, 4, v2
	v_add_u32_e32 v181, v2, v181
	v_bfe_i32 v2, v2, 27, 1
	s_waitcnt lgkmcnt(0)
	s_lshr_b32 s2, s2, 16
	v_lshrrev_b32_e32 v2, 22, v2
	s_cmp_lg_u32 s2, 0
	v_add_u32_e32 v2, v180, v2
	s_cselect_b64 s[2:3], -1, 0
	v_and_b32_e32 v2, 0xfffffc00, v2
	s_cmp_lg_u64 s[2:3], 0
	v_sub_u32_e32 v2, v180, v2
	s_addc_u32 s16, s4, s15
	s_lshr_b32 s3, s15, 3
	v_lshrrev_b32_e32 v180, 4, v2
	s_and_b32 s2, s15, 7
	s_add_i32 s4, s3, 0xffffff28
	v_bitop3_b32 v2, v180, v2, 32 bitop3:0x6c
	s_cmpk_lt_u32 s15, 0x6c0
	v_ashrrev_i32_e32 v182, 31, v2
	s_cselect_b32 s3, s3, s4
	s_cmpk_gt_u32 s15, 0x6bf
	v_lshrrev_b32_e32 v182, 26, v182
	s_cselect_b32 s4, 8, 0
	s_and_b32 s5, s3, 7
	v_add_u32_e32 v182, v2, v182
	s_or_b32 s4, s5, s4
	v_lshrrev_b32_e32 v183, 6, v182
	v_and_b32_e32 v182, 0xc0, v182
	s_lshr_b32 s82, s3, 3
	s_lshl_b32 s3, s4, 3
	v_ashrrev_i32_e32 v181, 6, v181
	v_sub_u32_e32 v2, v2, v182
	s_or_b32 s14, s3, s2
	v_lshlrev_b32_e32 v180, 3, v181
	v_lshlrev_b32_e32 v181, 5, v181
	v_ashrrev_i16_sdwa v2, v196, sext(v2) dst_sel:DWORD dst_unused:UNUSED_PAD src0_sel:DWORD src1_sel:BYTE_0
	s_lshl_b64 s[2:3], s[82:83], 18
	v_and_b32_e32 v180, 0x3ffff0, v180
	v_and_b32_e32 v181, 32, v181
	v_bfe_i32 v2, v2, 0, 16
	s_add_u32 s4, s19, s2
	s_addc_u32 s5, s22, s3
	s_lshl_b32 s2, s14, 18
	v_add_lshl_u32 v180, v183, v180, 10
	v_add_lshl_u32 v2, v181, v2, 1
	v_add3_u32 v180, v180, s2, v2
	v_add_u32_e32 v181, 0x10000, v180
	v_add_u32_e32 v182, 0x20000, v180
	v_add_u32_e32 v183, 0x30000, v180
	s_mov_b64 s[6:7], s[8:9]
	s_mov_b32 s15, s16
	s_mov_b32 s16, s82
	s_branch .LBB0_257

.LBB0_902:
	ds_read_b128 v[20:23], v186
	ds_read_b128 v[24:27], v186 offset:1024
	ds_read_b128 v[28:31], v186 offset:2048
	ds_read_b128 v[32:35], v186 offset:3072
	ds_read_b128 v[4:7], v187
	ds_read_b128 v[8:11], v187 offset:1024
	ds_read_b128 v[12:15], v187 offset:2048
	ds_read_b128 v[16:19], v187 offset:3072
	v_add_u32_e32 v165, 0xc000, v172
	s_add_u32 s2, s34, 0x80
	v_mov_b32_e32 v164, v176
	v_readfirstlane_b32 s13, v165
	v_add_u32_e32 v165, 0xe000, v172
	ds_read_b128 v[204:207], v188
	ds_read_b128 v[208:211], v188 offset:1024
	ds_read_b128 v[212:215], v189
	ds_read_b128 v[216:219], v189 offset:1024
	ds_read_b128 v[220:223], v190
	ds_read_b128 v[224:227], v190 offset:1024
	ds_read_b128 v[228:231], v191
	ds_read_b128 v[232:235], v191 offset:1024
	s_addc_u32 s3, s35, 0
	s_mov_b32 m0, s13
	v_readfirstlane_b32 s12, v165
	global_load_lds_dwordx4 v164, s[2:3]
	v_mov_b32_e32 v164, v178
	s_mov_b32 m0, s12
	s_nop 0
	global_load_lds_dwordx4 v164, s[2:3]
	s_waitcnt vmcnt(8)
	s_waitcnt lgkmcnt(0)
	s_barrier
	s_waitcnt lgkmcnt(0)
	v_mfma_scale_f32_16x16x128_f8f6f4 v[160:163], v[20:27], v[204:211], v[160:163], v166, v167 op_sel_hi:[0,0,0]
	v_mfma_scale_f32_16x16x128_f8f6f4 v[156:159], v[28:35], v[204:211], v[156:159], v166, v167 op_sel_hi:[0,0,0]
	v_mfma_scale_f32_16x16x128_f8f6f4 v[152:155], v[20:27], v[212:219], v[152:155], v166, v167 op_sel_hi:[0,0,0]
	v_mfma_scale_f32_16x16x128_f8f6f4 v[148:151], v[28:35], v[212:219], v[148:151], v166, v167 op_sel_hi:[0,0,0]
	v_mfma_scale_f32_16x16x128_f8f6f4 v[144:147], v[20:27], v[220:227], v[144:147], v166, v167 op_sel_hi:[0,0,0]
	v_mfma_scale_f32_16x16x128_f8f6f4 v[140:143], v[28:35], v[220:227], v[140:143], v166, v167 op_sel_hi:[0,0,0]
	v_mfma_scale_f32_16x16x128_f8f6f4 v[136:139], v[20:27], v[228:235], v[136:139], v166, v167 op_sel_hi:[0,0,0]
	v_mfma_scale_f32_16x16x128_f8f6f4 v[132:135], v[28:35], v[228:235], v[132:135], v166, v167 op_sel_hi:[0,0,0]
	v_mfma_scale_f32_16x16x128_f8f6f4 v[128:131], v[4:11], v[204:211], v[128:131], v166, v167 op_sel_hi:[0,0,0]
	v_mfma_scale_f32_16x16x128_f8f6f4 v[124:127], v[12:19], v[204:211], v[124:127], v166, v167 op_sel_hi:[0,0,0]
	v_mfma_scale_f32_16x16x128_f8f6f4 v[120:123], v[4:11], v[212:219], v[120:123], v166, v167 op_sel_hi:[0,0,0]
	v_mfma_scale_f32_16x16x128_f8f6f4 v[116:119], v[12:19], v[212:219], v[116:119], v166, v167 op_sel_hi:[0,0,0]
	v_mfma_scale_f32_16x16x128_f8f6f4 v[112:115], v[4:11], v[220:227], v[112:115], v166, v167 op_sel_hi:[0,0,0]
	v_mfma_scale_f32_16x16x128_f8f6f4 v[108:111], v[12:19], v[220:227], v[108:111], v166, v167 op_sel_hi:[0,0,0]
	v_mfma_scale_f32_16x16x128_f8f6f4 v[104:107], v[4:11], v[228:235], v[104:107], v166, v167 op_sel_hi:[0,0,0]
	v_mfma_scale_f32_16x16x128_f8f6f4 v[100:103], v[12:19], v[228:235], v[100:103], v166, v167 op_sel_hi:[0,0,0]
	s_barrier
	s_add_u32 s2, s6, 0x100
	v_mov_b32_e32 v164, v2
	v_readfirstlane_b32 s23, v168
	ds_read_b128 v[204:207], v188 offset:16384
	ds_read_b128 v[208:211], v188 offset:17408
	ds_read_b128 v[212:215], v189 offset:16384
	ds_read_b128 v[216:219], v189 offset:17408
	ds_read_b128 v[220:223], v190 offset:16384
	ds_read_b128 v[224:227], v190 offset:17408
	ds_read_b128 v[228:231], v191 offset:16384
	ds_read_b128 v[232:235], v191 offset:17408
	s_addc_u32 s3, s7, 0
	s_mov_b32 m0, s23
	v_readfirstlane_b32 s23, v169
	global_load_lds_dwordx4 v164, s[2:3]
	s_add_u32 s2, s6, 0x8100
	v_mov_b32_e32 v164, v2
	s_addc_u32 s3, s7, 0
	s_mov_b32 m0, s23
	v_readfirstlane_b32 s23, v170
	global_load_lds_dwordx4 v164, s[2:3]
	s_add_u32 s2, s6, 0x10100
	v_mov_b32_e32 v164, v2
	s_addc_u32 s3, s7, 0
	s_mov_b32 m0, s23
	v_readfirstlane_b32 s23, v171
	global_load_lds_dwordx4 v164, s[2:3]
	s_add_u32 s2, s6, 0x18100
	v_mov_b32_e32 v164, v2
	s_addc_u32 s3, s7, 0
	s_mov_b32 m0, s23
	v_readfirstlane_b32 s23, v172
	global_load_lds_dwordx4 v164, s[2:3]
	s_add_u32 s2, s34, 0x100
	v_mov_b32_e32 v164, v173
	s_addc_u32 s3, s35, 0
	s_mov_b32 m0, s23
	v_readfirstlane_b32 s23, v174
	global_load_lds_dwordx4 v164, s[2:3]
	v_mov_b32_e32 v164, v175
	s_mov_b32 m0, s23
	s_nop 0
	global_load_lds_dwordx4 v164, s[2:3]
	s_waitcnt vmcnt(8)
	s_waitcnt lgkmcnt(0)
	s_barrier
	s_waitcnt lgkmcnt(0)
	v_mfma_scale_f32_16x16x128_f8f6f4 v[96:99], v[20:27], v[204:211], v[96:99], v166, v167 op_sel_hi:[0,0,0]
	v_mfma_scale_f32_16x16x128_f8f6f4 v[92:95], v[28:35], v[204:211], v[92:95], v166, v167 op_sel_hi:[0,0,0]
	v_mfma_scale_f32_16x16x128_f8f6f4 v[88:91], v[20:27], v[212:219], v[88:91], v166, v167 op_sel_hi:[0,0,0]
	v_mfma_scale_f32_16x16x128_f8f6f4 v[84:87], v[28:35], v[212:219], v[84:87], v166, v167 op_sel_hi:[0,0,0]
	v_mfma_scale_f32_16x16x128_f8f6f4 v[80:83], v[20:27], v[220:227], v[80:83], v166, v167 op_sel_hi:[0,0,0]
	v_mfma_scale_f32_16x16x128_f8f6f4 v[76:79], v[28:35], v[220:227], v[76:79], v166, v167 op_sel_hi:[0,0,0]
	v_mfma_scale_f32_16x16x128_f8f6f4 v[72:75], v[20:27], v[228:235], v[72:75], v166, v167 op_sel_hi:[0,0,0]
	v_mfma_scale_f32_16x16x128_f8f6f4 v[68:71], v[28:35], v[228:235], v[68:71], v166, v167 op_sel_hi:[0,0,0]
	v_mfma_scale_f32_16x16x128_f8f6f4 v[64:67], v[4:11], v[204:211], v[64:67], v166, v167 op_sel_hi:[0,0,0]
	v_mfma_scale_f32_16x16x128_f8f6f4 v[60:63], v[12:19], v[204:211], v[60:63], v166, v167 op_sel_hi:[0,0,0]
	v_mfma_scale_f32_16x16x128_f8f6f4 v[56:59], v[4:11], v[212:219], v[56:59], v166, v167 op_sel_hi:[0,0,0]
	v_mfma_scale_f32_16x16x128_f8f6f4 v[52:55], v[12:19], v[212:219], v[52:55], v166, v167 op_sel_hi:[0,0,0]
	v_mfma_scale_f32_16x16x128_f8f6f4 v[48:51], v[4:11], v[220:227], v[48:51], v166, v167 op_sel_hi:[0,0,0]
	v_mfma_scale_f32_16x16x128_f8f6f4 v[44:47], v[12:19], v[220:227], v[44:47], v166, v167 op_sel_hi:[0,0,0]
	v_mfma_scale_f32_16x16x128_f8f6f4 v[40:43], v[4:11], v[228:235], v[40:43], v166, v167 op_sel_hi:[0,0,0]
	v_mfma_scale_f32_16x16x128_f8f6f4 v[36:39], v[12:19], v[228:235], v[36:39], v166, v167 op_sel_hi:[0,0,0]
	s_barrier
	ds_read_b128 v[20:23], v201
	ds_read_b128 v[24:27], v201 offset:1024
	ds_read_b128 v[28:31], v201 offset:2048
	ds_read_b128 v[32:35], v201 offset:3072
	ds_read_b128 v[4:7], v202
	ds_read_b128 v[8:11], v202 offset:1024
	ds_read_b128 v[12:15], v202 offset:2048
	ds_read_b128 v[16:19], v202 offset:3072
	v_mov_b32_e32 v164, v176
	v_readfirstlane_b32 s23, v177
	ds_read_b128 v[204:207], v188 offset:32768
	ds_read_b128 v[208:211], v188 offset:33792
	ds_read_b128 v[212:215], v189 offset:32768
	ds_read_b128 v[216:219], v189 offset:33792
	ds_read_b128 v[220:223], v190 offset:32768
	ds_read_b128 v[224:227], v190 offset:33792
	ds_read_b128 v[228:231], v191 offset:32768
	ds_read_b128 v[232:235], v191 offset:33792
	s_mov_b32 m0, s23
	v_readfirstlane_b32 s23, v179
	global_load_lds_dwordx4 v164, s[2:3]
	v_mov_b32_e32 v164, v178
	s_mov_b32 m0, s23
	s_nop 0
	global_load_lds_dwordx4 v164, s[2:3]
	s_waitcnt vmcnt(8)
	s_waitcnt lgkmcnt(0)
	s_barrier
	s_waitcnt lgkmcnt(0)
	v_mfma_scale_f32_16x16x128_f8f6f4 v[160:163], v[20:27], v[204:211], v[160:163], v166, v167 op_sel_hi:[0,0,0]
	v_mfma_scale_f32_16x16x128_f8f6f4 v[156:159], v[28:35], v[204:211], v[156:159], v166, v167 op_sel_hi:[0,0,0]
	v_mfma_scale_f32_16x16x128_f8f6f4 v[152:155], v[20:27], v[212:219], v[152:155], v166, v167 op_sel_hi:[0,0,0]
	v_mfma_scale_f32_16x16x128_f8f6f4 v[148:151], v[28:35], v[212:219], v[148:151], v166, v167 op_sel_hi:[0,0,0]
	v_mfma_scale_f32_16x16x128_f8f6f4 v[144:147], v[20:27], v[220:227], v[144:147], v166, v167 op_sel_hi:[0,0,0]
	v_mfma_scale_f32_16x16x128_f8f6f4 v[140:143], v[28:35], v[220:227], v[140:143], v166, v167 op_sel_hi:[0,0,0]
	v_mfma_scale_f32_16x16x128_f8f6f4 v[136:139], v[20:27], v[228:235], v[136:139], v166, v167 op_sel_hi:[0,0,0]
	v_mfma_scale_f32_16x16x128_f8f6f4 v[132:135], v[28:35], v[228:235], v[132:135], v166, v167 op_sel_hi:[0,0,0]
	v_mfma_scale_f32_16x16x128_f8f6f4 v[128:131], v[4:11], v[204:211], v[128:131], v166, v167 op_sel_hi:[0,0,0]
	v_mfma_scale_f32_16x16x128_f8f6f4 v[124:127], v[12:19], v[204:211], v[124:127], v166, v167 op_sel_hi:[0,0,0]
	v_mfma_scale_f32_16x16x128_f8f6f4 v[120:123], v[4:11], v[212:219], v[120:123], v166, v167 op_sel_hi:[0,0,0]
	v_mfma_scale_f32_16x16x128_f8f6f4 v[116:119], v[12:19], v[212:219], v[116:119], v166, v167 op_sel_hi:[0,0,0]
	v_mfma_scale_f32_16x16x128_f8f6f4 v[112:115], v[4:11], v[220:227], v[112:115], v166, v167 op_sel_hi:[0,0,0]
	v_mfma_scale_f32_16x16x128_f8f6f4 v[108:111], v[12:19], v[220:227], v[108:111], v166, v167 op_sel_hi:[0,0,0]
	v_mfma_scale_f32_16x16x128_f8f6f4 v[104:107], v[4:11], v[228:235], v[104:107], v166, v167 op_sel_hi:[0,0,0]
	v_mfma_scale_f32_16x16x128_f8f6f4 v[100:103], v[12:19], v[228:235], v[100:103], v166, v167 op_sel_hi:[0,0,0]
	s_barrier
	s_add_u32 s2, s6, 0x180
	v_mov_b32_e32 v164, v2
	v_readfirstlane_b32 s23, v180
	ds_read_b128 v[204:207], v188 offset:49152
	ds_read_b128 v[208:211], v188 offset:50176
	ds_read_b128 v[212:215], v189 offset:49152
	ds_read_b128 v[216:219], v189 offset:50176
	ds_read_b128 v[220:223], v190 offset:49152
	ds_read_b128 v[224:227], v190 offset:50176
	ds_read_b128 v[228:231], v191 offset:49152
	ds_read_b128 v[232:235], v191 offset:50176
	s_addc_u32 s3, s7, 0
	s_mov_b32 m0, s23
	v_readfirstlane_b32 s23, v181
	global_load_lds_dwordx4 v164, s[2:3]
	s_add_u32 s2, s6, 0x8180
	v_mov_b32_e32 v164, v2
	s_addc_u32 s3, s7, 0
	s_mov_b32 m0, s23
	v_readfirstlane_b32 s23, v184
	global_load_lds_dwordx4 v164, s[2:3]
	s_add_u32 s2, s6, 0x10180
	v_mov_b32_e32 v164, v2
	s_addc_u32 s3, s7, 0
	s_mov_b32 m0, s23
	v_readfirstlane_b32 s23, v185
	global_load_lds_dwordx4 v164, s[2:3]
	s_add_u32 s2, s6, 0x18180
	v_mov_b32_e32 v164, v2
	s_addc_u32 s3, s7, 0
	s_mov_b32 m0, s23
	v_readfirstlane_b32 s23, v182
	global_load_lds_dwordx4 v164, s[2:3]
	s_add_u32 s2, s34, 0x180
	v_mov_b32_e32 v164, v173
	s_addc_u32 s3, s35, 0
	s_mov_b32 m0, s23
	v_readfirstlane_b32 s23, v183
	global_load_lds_dwordx4 v164, s[2:3]
	v_mov_b32_e32 v164, v175
	s_mov_b32 m0, s23
	s_nop 0
	global_load_lds_dwordx4 v164, s[2:3]
	s_waitcnt vmcnt(8)
	s_waitcnt lgkmcnt(0)
	s_barrier
	s_waitcnt lgkmcnt(0)
	v_mfma_scale_f32_16x16x128_f8f6f4 v[96:99], v[20:27], v[204:211], v[96:99], v166, v167 op_sel_hi:[0,0,0]
	v_mfma_scale_f32_16x16x128_f8f6f4 v[92:95], v[28:35], v[204:211], v[92:95], v166, v167 op_sel_hi:[0,0,0]
	v_mfma_scale_f32_16x16x128_f8f6f4 v[88:91], v[20:27], v[212:219], v[88:91], v166, v167 op_sel_hi:[0,0,0]
	v_mfma_scale_f32_16x16x128_f8f6f4 v[84:87], v[28:35], v[212:219], v[84:87], v166, v167 op_sel_hi:[0,0,0]
	v_mfma_scale_f32_16x16x128_f8f6f4 v[80:83], v[20:27], v[220:227], v[80:83], v166, v167 op_sel_hi:[0,0,0]
	v_mfma_scale_f32_16x16x128_f8f6f4 v[76:79], v[28:35], v[220:227], v[76:79], v166, v167 op_sel_hi:[0,0,0]
	v_mfma_scale_f32_16x16x128_f8f6f4 v[72:75], v[20:27], v[228:235], v[72:75], v166, v167 op_sel_hi:[0,0,0]
	v_mfma_scale_f32_16x16x128_f8f6f4 v[68:71], v[28:35], v[228:235], v[68:71], v166, v167 op_sel_hi:[0,0,0]
	v_mfma_scale_f32_16x16x128_f8f6f4 v[64:67], v[4:11], v[204:211], v[64:67], v166, v167 op_sel_hi:[0,0,0]
	v_mfma_scale_f32_16x16x128_f8f6f4 v[60:63], v[12:19], v[204:211], v[60:63], v166, v167 op_sel_hi:[0,0,0]
	v_mfma_scale_f32_16x16x128_f8f6f4 v[56:59], v[4:11], v[212:219], v[56:59], v166, v167 op_sel_hi:[0,0,0]
	v_mfma_scale_f32_16x16x128_f8f6f4 v[52:55], v[12:19], v[212:219], v[52:55], v166, v167 op_sel_hi:[0,0,0]
	v_mfma_scale_f32_16x16x128_f8f6f4 v[48:51], v[4:11], v[220:227], v[48:51], v166, v167 op_sel_hi:[0,0,0]
	v_mfma_scale_f32_16x16x128_f8f6f4 v[44:47], v[12:19], v[220:227], v[44:47], v166, v167 op_sel_hi:[0,0,0]
	v_mfma_scale_f32_16x16x128_f8f6f4 v[40:43], v[4:11], v[228:235], v[40:43], v166, v167 op_sel_hi:[0,0,0]
	v_mfma_scale_f32_16x16x128_f8f6f4 v[36:39], v[12:19], v[228:235], v[36:39], v166, v167 op_sel_hi:[0,0,0]
	s_barrier
	ds_read_b128 v[20:23], v186
	ds_read_b128 v[24:27], v186 offset:1024
	ds_read_b128 v[28:31], v186 offset:2048
	ds_read_b128 v[32:35], v186 offset:3072
	ds_read_b128 v[4:7], v187
	ds_read_b128 v[8:11], v187 offset:1024
	ds_read_b128 v[12:15], v187 offset:2048
	ds_read_b128 v[16:19], v187 offset:3072
	v_mov_b32_e32 v164, v176
	s_mov_b32 m0, s13
	ds_read_b128 v[204:207], v188
	ds_read_b128 v[208:211], v188 offset:1024
	ds_read_b128 v[212:215], v189
	ds_read_b128 v[216:219], v189 offset:1024
	ds_read_b128 v[220:223], v190
	ds_read_b128 v[224:227], v190 offset:1024
	ds_read_b128 v[228:231], v191
	ds_read_b128 v[232:235], v191 offset:1024
	s_nop 0
	global_load_lds_dwordx4 v164, s[2:3]
	v_mov_b32_e32 v164, v178
	s_mov_b32 m0, s12
	s_nop 0
	global_load_lds_dwordx4 v164, s[2:3]
	s_waitcnt vmcnt(8)
	s_waitcnt lgkmcnt(0)
	s_barrier
	s_waitcnt lgkmcnt(0)
	v_mfma_scale_f32_16x16x128_f8f6f4 v[160:163], v[20:27], v[204:211], v[160:163], v166, v167 op_sel_hi:[0,0,0]
	v_mfma_scale_f32_16x16x128_f8f6f4 v[156:159], v[28:35], v[204:211], v[156:159], v166, v167 op_sel_hi:[0,0,0]
	v_mfma_scale_f32_16x16x128_f8f6f4 v[152:155], v[20:27], v[212:219], v[152:155], v166, v167 op_sel_hi:[0,0,0]
	v_mfma_scale_f32_16x16x128_f8f6f4 v[148:151], v[28:35], v[212:219], v[148:151], v166, v167 op_sel_hi:[0,0,0]
	v_mfma_scale_f32_16x16x128_f8f6f4 v[144:147], v[20:27], v[220:227], v[144:147], v166, v167 op_sel_hi:[0,0,0]
	v_mfma_scale_f32_16x16x128_f8f6f4 v[140:143], v[28:35], v[220:227], v[140:143], v166, v167 op_sel_hi:[0,0,0]
	v_mfma_scale_f32_16x16x128_f8f6f4 v[136:139], v[20:27], v[228:235], v[136:139], v166, v167 op_sel_hi:[0,0,0]
	v_mfma_scale_f32_16x16x128_f8f6f4 v[132:135], v[28:35], v[228:235], v[132:135], v166, v167 op_sel_hi:[0,0,0]
	v_mfma_scale_f32_16x16x128_f8f6f4 v[128:131], v[4:11], v[204:211], v[128:131], v166, v167 op_sel_hi:[0,0,0]
	v_mfma_scale_f32_16x16x128_f8f6f4 v[124:127], v[12:19], v[204:211], v[124:127], v166, v167 op_sel_hi:[0,0,0]
	v_mfma_scale_f32_16x16x128_f8f6f4 v[120:123], v[4:11], v[212:219], v[120:123], v166, v167 op_sel_hi:[0,0,0]
	v_mfma_scale_f32_16x16x128_f8f6f4 v[116:119], v[12:19], v[212:219], v[116:119], v166, v167 op_sel_hi:[0,0,0]
	v_mfma_scale_f32_16x16x128_f8f6f4 v[112:115], v[4:11], v[220:227], v[112:115], v166, v167 op_sel_hi:[0,0,0]
	v_mfma_scale_f32_16x16x128_f8f6f4 v[108:111], v[12:19], v[220:227], v[108:111], v166, v167 op_sel_hi:[0,0,0]
	v_mfma_scale_f32_16x16x128_f8f6f4 v[104:107], v[4:11], v[228:235], v[104:107], v166, v167 op_sel_hi:[0,0,0]
	v_mfma_scale_f32_16x16x128_f8f6f4 v[100:103], v[12:19], v[228:235], v[100:103], v166, v167 op_sel_hi:[0,0,0]
	s_barrier
	s_cmp_gt_i32 s22, 1
	s_cselect_b64 s[40:41], -1, 0
	s_cmp_lt_i32 s22, 2
	s_cbranch_scc1 .LBB0_907
	s_mov_b64 s[12:13], 0
	s_cmpk_lt_u32 s21, 0x200
	s_mov_b32 s23, s21
	s_mov_b64 s[2:3], 0
	s_cbranch_scc0 .LBB0_905
	s_lshr_b32 s3, s21, 3
	s_add_i32 s23, s18, s21
	s_and_b32 s2, s21, 7
	s_sub_i32 s19, s3, 32
	s_cmpk_lt_u32 s21, 0x100
	s_cselect_b32 s3, s3, s19
	s_lshr_b32 s19, s21, 5
	s_and_b32 s19, s19, 8
	s_and_b32 s24, s3, 7
	s_or_b32 s19, s24, s19
	s_lshr_b32 s24, s3, 3
	s_lshl_b32 s3, s19, 3
	s_or_b32 s19, s3, s2
	s_mov_b64 s[2:3], -1
	s_mov_b32 s82, 0
	s_and_b64 vcc, exec, s[12:13]
	s_cbranch_vccz .LBB0_908
	s_branch .LBB0_906

.LBB0_910:
	v_mov_b32_e32 v164, v2
	v_readfirstlane_b32 s2, v168
	ds_read_b128 v[204:207], v188 offset:16384
	ds_read_b128 v[208:211], v188 offset:17408
	ds_read_b128 v[212:215], v189 offset:16384
	ds_read_b128 v[216:219], v189 offset:17408
	ds_read_b128 v[220:223], v190 offset:16384
	ds_read_b128 v[224:227], v190 offset:17408
	ds_read_b128 v[228:231], v191 offset:16384
	ds_read_b128 v[232:235], v191 offset:17408
	s_mov_b32 m0, s2
	s_add_u32 s2, s6, 0x8000
	global_load_lds_dwordx4 v164, s[6:7]
	v_mov_b32_e32 v164, v2
	v_readfirstlane_b32 s21, v169
	s_addc_u32 s3, s7, 0
	s_mov_b32 m0, s21
	v_readfirstlane_b32 s21, v170
	global_load_lds_dwordx4 v164, s[2:3]
	s_add_u32 s2, s6, 0x10000
	v_mov_b32_e32 v164, v2
	s_addc_u32 s3, s7, 0
	s_mov_b32 m0, s21
	v_readfirstlane_b32 s21, v171
	global_load_lds_dwordx4 v164, s[2:3]
	s_add_u32 s2, s6, 0x18000
	v_mov_b32_e32 v164, v2
	s_addc_u32 s3, s7, 0
	s_mov_b32 m0, s21
	s_nop 0
	global_load_lds_dwordx4 v164, s[2:3]
	v_mov_b32_e32 v164, v173
	v_readfirstlane_b32 s2, v172
	s_mov_b32 m0, s2
	v_readfirstlane_b32 s2, v174
	global_load_lds_dwordx4 v164, s[34:35]
	v_mov_b32_e32 v164, v175
	s_mov_b32 m0, s2
	s_nop 0
	global_load_lds_dwordx4 v164, s[34:35]
	s_waitcnt vmcnt(8)
	s_waitcnt lgkmcnt(0)
	s_barrier
	s_waitcnt lgkmcnt(0)
	v_mfma_scale_f32_16x16x128_f8f6f4 v[96:99], v[20:27], v[204:211], v[96:99], v166, v167 op_sel_hi:[0,0,0]
	v_mfma_scale_f32_16x16x128_f8f6f4 v[92:95], v[28:35], v[204:211], v[92:95], v166, v167 op_sel_hi:[0,0,0]
	v_mfma_scale_f32_16x16x128_f8f6f4 v[88:91], v[20:27], v[212:219], v[88:91], v166, v167 op_sel_hi:[0,0,0]
	v_mfma_scale_f32_16x16x128_f8f6f4 v[84:87], v[28:35], v[212:219], v[84:87], v166, v167 op_sel_hi:[0,0,0]
	v_mfma_scale_f32_16x16x128_f8f6f4 v[80:83], v[20:27], v[220:227], v[80:83], v166, v167 op_sel_hi:[0,0,0]
	v_mfma_scale_f32_16x16x128_f8f6f4 v[76:79], v[28:35], v[220:227], v[76:79], v166, v167 op_sel_hi:[0,0,0]
	v_mfma_scale_f32_16x16x128_f8f6f4 v[72:75], v[20:27], v[228:235], v[72:75], v166, v167 op_sel_hi:[0,0,0]
	v_mfma_scale_f32_16x16x128_f8f6f4 v[68:71], v[28:35], v[228:235], v[68:71], v166, v167 op_sel_hi:[0,0,0]
	v_mfma_scale_f32_16x16x128_f8f6f4 v[64:67], v[4:11], v[204:211], v[64:67], v166, v167 op_sel_hi:[0,0,0]
	v_mfma_scale_f32_16x16x128_f8f6f4 v[60:63], v[12:19], v[204:211], v[60:63], v166, v167 op_sel_hi:[0,0,0]
	v_mfma_scale_f32_16x16x128_f8f6f4 v[56:59], v[4:11], v[212:219], v[56:59], v166, v167 op_sel_hi:[0,0,0]
	v_mfma_scale_f32_16x16x128_f8f6f4 v[52:55], v[12:19], v[212:219], v[52:55], v166, v167 op_sel_hi:[0,0,0]
	v_mfma_scale_f32_16x16x128_f8f6f4 v[48:51], v[4:11], v[220:227], v[48:51], v166, v167 op_sel_hi:[0,0,0]
	v_mfma_scale_f32_16x16x128_f8f6f4 v[44:47], v[12:19], v[220:227], v[44:47], v166, v167 op_sel_hi:[0,0,0]
	v_mfma_scale_f32_16x16x128_f8f6f4 v[40:43], v[4:11], v[228:235], v[40:43], v166, v167 op_sel_hi:[0,0,0]
	v_mfma_scale_f32_16x16x128_f8f6f4 v[36:39], v[12:19], v[228:235], v[36:39], v166, v167 op_sel_hi:[0,0,0]
	s_barrier
	ds_read_b128 v[20:23], v201
	ds_read_b128 v[24:27], v201 offset:1024
	ds_read_b128 v[28:31], v201 offset:2048
	ds_read_b128 v[32:35], v201 offset:3072
	ds_read_b128 v[4:7], v202
	ds_read_b128 v[8:11], v202 offset:1024
	ds_read_b128 v[12:15], v202 offset:2048
	ds_read_b128 v[16:19], v202 offset:3072
	v_mov_b32_e32 v164, v176
	v_readfirstlane_b32 s2, v177
	ds_read_b128 v[204:207], v188 offset:32768
	ds_read_b128 v[208:211], v188 offset:33792
	ds_read_b128 v[212:215], v189 offset:32768
	ds_read_b128 v[216:219], v189 offset:33792
	ds_read_b128 v[220:223], v190 offset:32768
	ds_read_b128 v[224:227], v190 offset:33792
	ds_read_b128 v[228:231], v191 offset:32768
	ds_read_b128 v[232:235], v191 offset:33792
	s_mov_b32 m0, s2
	v_readfirstlane_b32 s2, v179
	global_load_lds_dwordx4 v164, s[34:35]
	v_mov_b32_e32 v164, v178
	s_mov_b32 m0, s2
	s_nop 0
	global_load_lds_dwordx4 v164, s[34:35]
	s_waitcnt vmcnt(8)
	s_waitcnt lgkmcnt(0)
	s_barrier
	s_waitcnt lgkmcnt(0)
	v_mfma_scale_f32_16x16x128_f8f6f4 v[160:163], v[20:27], v[204:211], v[160:163], v166, v167 op_sel_hi:[0,0,0]
	v_mfma_scale_f32_16x16x128_f8f6f4 v[156:159], v[28:35], v[204:211], v[156:159], v166, v167 op_sel_hi:[0,0,0]
	v_mfma_scale_f32_16x16x128_f8f6f4 v[152:155], v[20:27], v[212:219], v[152:155], v166, v167 op_sel_hi:[0,0,0]
	v_mfma_scale_f32_16x16x128_f8f6f4 v[148:151], v[28:35], v[212:219], v[148:151], v166, v167 op_sel_hi:[0,0,0]
	v_mfma_scale_f32_16x16x128_f8f6f4 v[144:147], v[20:27], v[220:227], v[144:147], v166, v167 op_sel_hi:[0,0,0]
	v_mfma_scale_f32_16x16x128_f8f6f4 v[140:143], v[28:35], v[220:227], v[140:143], v166, v167 op_sel_hi:[0,0,0]
	v_mfma_scale_f32_16x16x128_f8f6f4 v[136:139], v[20:27], v[228:235], v[136:139], v166, v167 op_sel_hi:[0,0,0]
	v_mfma_scale_f32_16x16x128_f8f6f4 v[132:135], v[28:35], v[228:235], v[132:135], v166, v167 op_sel_hi:[0,0,0]
	v_mfma_scale_f32_16x16x128_f8f6f4 v[128:131], v[4:11], v[204:211], v[128:131], v166, v167 op_sel_hi:[0,0,0]
	v_mfma_scale_f32_16x16x128_f8f6f4 v[124:127], v[12:19], v[204:211], v[124:127], v166, v167 op_sel_hi:[0,0,0]
	v_mfma_scale_f32_16x16x128_f8f6f4 v[120:123], v[4:11], v[212:219], v[120:123], v166, v167 op_sel_hi:[0,0,0]
	v_mfma_scale_f32_16x16x128_f8f6f4 v[116:119], v[12:19], v[212:219], v[116:119], v166, v167 op_sel_hi:[0,0,0]
	v_mfma_scale_f32_16x16x128_f8f6f4 v[112:115], v[4:11], v[220:227], v[112:115], v166, v167 op_sel_hi:[0,0,0]
	v_mfma_scale_f32_16x16x128_f8f6f4 v[108:111], v[12:19], v[220:227], v[108:111], v166, v167 op_sel_hi:[0,0,0]
	v_mfma_scale_f32_16x16x128_f8f6f4 v[104:107], v[4:11], v[228:235], v[104:107], v166, v167 op_sel_hi:[0,0,0]
	v_mfma_scale_f32_16x16x128_f8f6f4 v[100:103], v[12:19], v[228:235], v[100:103], v166, v167 op_sel_hi:[0,0,0]
	s_barrier
	s_add_u32 s2, s6, 0x80
	v_mov_b32_e32 v164, v2
	v_readfirstlane_b32 s21, v180
	ds_read_b128 v[204:207], v188 offset:49152
	ds_read_b128 v[208:211], v188 offset:50176
	ds_read_b128 v[212:215], v189 offset:49152
	ds_read_b128 v[216:219], v189 offset:50176
	ds_read_b128 v[220:223], v190 offset:49152
	ds_read_b128 v[224:227], v190 offset:50176
	ds_read_b128 v[228:231], v191 offset:49152
	ds_read_b128 v[232:235], v191 offset:50176
	s_addc_u32 s3, s7, 0
	s_mov_b32 m0, s21
	v_readfirstlane_b32 s21, v181
	global_load_lds_dwordx4 v164, s[2:3]
	s_add_u32 s2, s6, 0x8080
	v_mov_b32_e32 v164, v2
	s_addc_u32 s3, s7, 0
	s_mov_b32 m0, s21
	v_readfirstlane_b32 s21, v184
	global_load_lds_dwordx4 v164, s[2:3]
	s_add_u32 s2, s6, 0x10080
	v_mov_b32_e32 v164, v2
	s_addc_u32 s3, s7, 0
	s_mov_b32 m0, s21
	v_readfirstlane_b32 s21, v185
	global_load_lds_dwordx4 v164, s[2:3]
	s_add_u32 s2, s6, 0x18080
	v_mov_b32_e32 v164, v2
	s_addc_u32 s3, s7, 0
	s_mov_b32 m0, s21
	v_readfirstlane_b32 s21, v182
	global_load_lds_dwordx4 v164, s[2:3]
	s_add_u32 s2, s34, 0x80
	v_mov_b32_e32 v164, v173
	s_addc_u32 s3, s35, 0
	s_mov_b32 m0, s21
	v_readfirstlane_b32 s21, v183
	global_load_lds_dwordx4 v164, s[2:3]
	v_mov_b32_e32 v164, v175
	s_mov_b32 m0, s21
	s_nop 0
	global_load_lds_dwordx4 v164, s[2:3]
	s_waitcnt vmcnt(8)
	s_waitcnt lgkmcnt(0)
	s_barrier
	s_waitcnt lgkmcnt(0)
	v_mfma_scale_f32_16x16x128_f8f6f4 v[96:99], v[20:27], v[204:211], v[96:99], v166, v167 op_sel_hi:[0,0,0]
	v_mfma_scale_f32_16x16x128_f8f6f4 v[92:95], v[28:35], v[204:211], v[92:95], v166, v167 op_sel_hi:[0,0,0]
	v_mfma_scale_f32_16x16x128_f8f6f4 v[88:91], v[20:27], v[212:219], v[88:91], v166, v167 op_sel_hi:[0,0,0]
	v_mfma_scale_f32_16x16x128_f8f6f4 v[84:87], v[28:35], v[212:219], v[84:87], v166, v167 op_sel_hi:[0,0,0]
	v_mfma_scale_f32_16x16x128_f8f6f4 v[80:83], v[20:27], v[220:227], v[80:83], v166, v167 op_sel_hi:[0,0,0]
	v_mfma_scale_f32_16x16x128_f8f6f4 v[76:79], v[28:35], v[220:227], v[76:79], v166, v167 op_sel_hi:[0,0,0]
	v_mfma_scale_f32_16x16x128_f8f6f4 v[72:75], v[20:27], v[228:235], v[72:75], v166, v167 op_sel_hi:[0,0,0]
	v_mfma_scale_f32_16x16x128_f8f6f4 v[68:71], v[28:35], v[228:235], v[68:71], v166, v167 op_sel_hi:[0,0,0]
	v_mfma_scale_f32_16x16x128_f8f6f4 v[64:67], v[4:11], v[204:211], v[64:67], v166, v167 op_sel_hi:[0,0,0]
	v_mfma_scale_f32_16x16x128_f8f6f4 v[60:63], v[12:19], v[204:211], v[60:63], v166, v167 op_sel_hi:[0,0,0]
	v_mfma_scale_f32_16x16x128_f8f6f4 v[56:59], v[4:11], v[212:219], v[56:59], v166, v167 op_sel_hi:[0,0,0]
	v_mfma_scale_f32_16x16x128_f8f6f4 v[52:55], v[12:19], v[212:219], v[52:55], v166, v167 op_sel_hi:[0,0,0]
	v_mfma_scale_f32_16x16x128_f8f6f4 v[48:51], v[4:11], v[220:227], v[48:51], v166, v167 op_sel_hi:[0,0,0]
	v_mfma_scale_f32_16x16x128_f8f6f4 v[44:47], v[12:19], v[220:227], v[44:47], v166, v167 op_sel_hi:[0,0,0]
	v_mfma_scale_f32_16x16x128_f8f6f4 v[40:43], v[4:11], v[228:235], v[40:43], v166, v167 op_sel_hi:[0,0,0]
	v_mfma_scale_f32_16x16x128_f8f6f4 v[36:39], v[12:19], v[228:235], v[36:39], v166, v167 op_sel_hi:[0,0,0]
	s_barrier
	s_and_saveexec_b64 s[2:3], s[38:39]
	s_cbranch_execz .LBB0_912
	s_barrier

.LBB0_1008:
	s_lshl_b64 s[2:3], s[82:83], 7
	s_add_u32 s26, s10, s2
	v_mov_b32_e32 v2, v201
	v_readfirstlane_b32 s28, v204
	ds_read_b128 v[180:183], v226 offset:16384
	ds_read_b128 v[184:187], v226 offset:17408
	ds_read_b128 v[188:191], v227 offset:16384
	ds_read_b128 v[192:195], v227 offset:17408
	ds_read_b128 v[230:233], v228 offset:16384
	ds_read_b128 v[234:237], v228 offset:17408
	ds_read_b128 v[238:241], v229 offset:16384
	ds_read_b128 v[242:245], v229 offset:17408
	s_addc_u32 s27, s11, s3
	s_mov_b32 m0, s28
	s_add_u32 s28, s26, 0x10000
	global_load_lds_dwordx4 v2, s[26:27]
	v_mov_b32_e32 v2, v201
	v_readfirstlane_b32 s30, v205
	s_addc_u32 s29, s27, 0
	s_mov_b32 m0, s30
	v_readfirstlane_b32 s30, v206
	global_load_lds_dwordx4 v2, s[28:29]
	s_add_u32 s28, s26, 0x20000
	v_mov_b32_e32 v2, v201
	s_addc_u32 s29, s27, 0
	s_mov_b32 m0, s30
	s_add_u32 s26, s26, 0x30000
	global_load_lds_dwordx4 v2, s[28:29]
	v_mov_b32_e32 v2, v201
	v_readfirstlane_b32 s28, v207
	s_addc_u32 s27, s27, 0
	s_mov_b32 m0, s28
	s_add_u32 s2, s8, s2
	global_load_lds_dwordx4 v2, s[26:27]
	v_mov_b32_e32 v2, v209
	v_readfirstlane_b32 s26, v208
	s_addc_u32 s3, s9, s3
	s_mov_b32 m0, s26
	v_readfirstlane_b32 s26, v213
	global_load_lds_dwordx4 v2, s[2:3]
	v_mov_b32_e32 v2, v210
	s_mov_b32 m0, s26
	s_nop 0
	global_load_lds_dwordx4 v2, s[2:3]
	s_waitcnt vmcnt(8)
	s_waitcnt lgkmcnt(0)
	s_barrier
	s_waitcnt lgkmcnt(0)
	v_mfma_scale_f32_16x16x128_f8f6f4 v[112:115], v[20:27], v[180:187], v[112:115], v202, v203 op_sel_hi:[0,0,0]
	v_mfma_scale_f32_16x16x128_f8f6f4 v[108:111], v[28:35], v[180:187], v[108:111], v202, v203 op_sel_hi:[0,0,0]
	v_mfma_scale_f32_16x16x128_f8f6f4 v[104:107], v[20:27], v[188:195], v[104:107], v202, v203 op_sel_hi:[0,0,0]
	v_mfma_scale_f32_16x16x128_f8f6f4 v[100:103], v[28:35], v[188:195], v[100:103], v202, v203 op_sel_hi:[0,0,0]
	v_mfma_scale_f32_16x16x128_f8f6f4 v[96:99], v[20:27], v[230:237], v[96:99], v202, v203 op_sel_hi:[0,0,0]
	v_mfma_scale_f32_16x16x128_f8f6f4 v[92:95], v[28:35], v[230:237], v[92:95], v202, v203 op_sel_hi:[0,0,0]
	v_mfma_scale_f32_16x16x128_f8f6f4 v[88:91], v[20:27], v[238:245], v[88:91], v202, v203 op_sel_hi:[0,0,0]
	v_mfma_scale_f32_16x16x128_f8f6f4 v[84:87], v[28:35], v[238:245], v[84:87], v202, v203 op_sel_hi:[0,0,0]
	v_mfma_scale_f32_16x16x128_f8f6f4 v[80:83], v[4:11], v[180:187], v[80:83], v202, v203 op_sel_hi:[0,0,0]
	v_mfma_scale_f32_16x16x128_f8f6f4 v[76:79], v[12:19], v[180:187], v[76:79], v202, v203 op_sel_hi:[0,0,0]
	v_mfma_scale_f32_16x16x128_f8f6f4 v[72:75], v[4:11], v[188:195], v[72:75], v202, v203 op_sel_hi:[0,0,0]
	v_mfma_scale_f32_16x16x128_f8f6f4 v[68:71], v[12:19], v[188:195], v[68:71], v202, v203 op_sel_hi:[0,0,0]
	v_mfma_scale_f32_16x16x128_f8f6f4 v[64:67], v[4:11], v[230:237], v[64:67], v202, v203 op_sel_hi:[0,0,0]
	v_mfma_scale_f32_16x16x128_f8f6f4 v[60:63], v[12:19], v[230:237], v[60:63], v202, v203 op_sel_hi:[0,0,0]
	v_mfma_scale_f32_16x16x128_f8f6f4 v[56:59], v[4:11], v[238:245], v[56:59], v202, v203 op_sel_hi:[0,0,0]
	v_mfma_scale_f32_16x16x128_f8f6f4 v[52:55], v[12:19], v[238:245], v[52:55], v202, v203 op_sel_hi:[0,0,0]
	s_barrier
	ds_read_b128 v[20:23], v224
	ds_read_b128 v[24:27], v224 offset:1024
	ds_read_b128 v[28:31], v224 offset:2048
	ds_read_b128 v[32:35], v224 offset:3072
	ds_read_b128 v[4:7], v225
	ds_read_b128 v[8:11], v225 offset:1024
	ds_read_b128 v[12:15], v225 offset:2048
	ds_read_b128 v[16:19], v225 offset:3072
	v_mov_b32_e32 v2, v211
	v_readfirstlane_b32 s26, v214
	ds_read_b128 v[180:183], v226 offset:32768
	ds_read_b128 v[184:187], v226 offset:33792
	ds_read_b128 v[188:191], v227 offset:32768
	ds_read_b128 v[192:195], v227 offset:33792
	ds_read_b128 v[230:233], v228 offset:32768
	ds_read_b128 v[234:237], v228 offset:33792
	ds_read_b128 v[238:241], v229 offset:32768
	ds_read_b128 v[242:245], v229 offset:33792
	s_mov_b32 m0, s26
	v_readfirstlane_b32 s26, v215
	global_load_lds_dwordx4 v2, s[2:3]
	v_mov_b32_e32 v2, v212
	s_mov_b32 m0, s26
	s_nop 0
	global_load_lds_dwordx4 v2, s[2:3]
	s_waitcnt vmcnt(8)
	s_waitcnt lgkmcnt(0)
	s_barrier
	s_waitcnt lgkmcnt(0)
	v_mfma_scale_f32_16x16x128_f8f6f4 v[176:179], v[20:27], v[180:187], v[176:179], v202, v203 op_sel_hi:[0,0,0]
	v_mfma_scale_f32_16x16x128_f8f6f4 v[172:175], v[28:35], v[180:187], v[172:175], v202, v203 op_sel_hi:[0,0,0]
	v_mfma_scale_f32_16x16x128_f8f6f4 v[168:171], v[20:27], v[188:195], v[168:171], v202, v203 op_sel_hi:[0,0,0]
	v_mfma_scale_f32_16x16x128_f8f6f4 v[164:167], v[28:35], v[188:195], v[164:167], v202, v203 op_sel_hi:[0,0,0]
	v_mfma_scale_f32_16x16x128_f8f6f4 v[160:163], v[20:27], v[230:237], v[160:163], v202, v203 op_sel_hi:[0,0,0]
	v_mfma_scale_f32_16x16x128_f8f6f4 v[156:159], v[28:35], v[230:237], v[156:159], v202, v203 op_sel_hi:[0,0,0]
	v_mfma_scale_f32_16x16x128_f8f6f4 v[152:155], v[20:27], v[238:245], v[152:155], v202, v203 op_sel_hi:[0,0,0]
	v_mfma_scale_f32_16x16x128_f8f6f4 v[148:151], v[28:35], v[238:245], v[148:151], v202, v203 op_sel_hi:[0,0,0]
	v_mfma_scale_f32_16x16x128_f8f6f4 v[144:147], v[4:11], v[180:187], v[144:147], v202, v203 op_sel_hi:[0,0,0]
	v_mfma_scale_f32_16x16x128_f8f6f4 v[140:143], v[12:19], v[180:187], v[140:143], v202, v203 op_sel_hi:[0,0,0]
	v_mfma_scale_f32_16x16x128_f8f6f4 v[136:139], v[4:11], v[188:195], v[136:139], v202, v203 op_sel_hi:[0,0,0]
	v_mfma_scale_f32_16x16x128_f8f6f4 v[132:135], v[12:19], v[188:195], v[132:135], v202, v203 op_sel_hi:[0,0,0]
	v_mfma_scale_f32_16x16x128_f8f6f4 v[128:131], v[4:11], v[230:237], v[128:131], v202, v203 op_sel_hi:[0,0,0]
	v_mfma_scale_f32_16x16x128_f8f6f4 v[124:127], v[12:19], v[230:237], v[124:127], v202, v203 op_sel_hi:[0,0,0]
	v_mfma_scale_f32_16x16x128_f8f6f4 v[120:123], v[4:11], v[238:245], v[120:123], v202, v203 op_sel_hi:[0,0,0]
	v_mfma_scale_f32_16x16x128_f8f6f4 v[116:119], v[12:19], v[238:245], v[116:119], v202, v203 op_sel_hi:[0,0,0]
	s_barrier
	s_add_i32 s82, s82, 1
	s_lshl_b64 s[2:3], s[82:83], 7
	s_add_u32 s26, s10, s2
	v_mov_b32_e32 v2, v201
	v_readfirstlane_b32 s28, v216
	ds_read_b128 v[180:183], v226 offset:49152
	ds_read_b128 v[184:187], v226 offset:50176
	ds_read_b128 v[188:191], v227 offset:49152
	ds_read_b128 v[192:195], v227 offset:50176
	ds_read_b128 v[230:233], v228 offset:49152
	ds_read_b128 v[234:237], v228 offset:50176
	ds_read_b128 v[238:241], v229 offset:49152
	ds_read_b128 v[242:245], v229 offset:50176
	s_addc_u32 s27, s11, s3
	s_mov_b32 m0, s28
	s_add_u32 s28, s26, 0x10000
	global_load_lds_dwordx4 v2, s[26:27]
	v_mov_b32_e32 v2, v201
	v_readfirstlane_b32 s30, v217
	s_addc_u32 s29, s27, 0
	s_mov_b32 m0, s30
	v_readfirstlane_b32 s30, v220
	global_load_lds_dwordx4 v2, s[28:29]
	s_add_u32 s28, s26, 0x20000
	v_mov_b32_e32 v2, v201
	s_addc_u32 s29, s27, 0
	s_mov_b32 m0, s30
	s_add_u32 s26, s26, 0x30000
	global_load_lds_dwordx4 v2, s[28:29]
	v_mov_b32_e32 v2, v201
	v_readfirstlane_b32 s28, v221
	s_addc_u32 s27, s27, 0
	s_mov_b32 m0, s28
	s_add_u32 s2, s8, s2
	global_load_lds_dwordx4 v2, s[26:27]
	v_mov_b32_e32 v2, v209
	v_readfirstlane_b32 s26, v218
	s_addc_u32 s3, s9, s3
	s_mov_b32 m0, s26
	v_readfirstlane_b32 s26, v219
	global_load_lds_dwordx4 v2, s[2:3]
	v_mov_b32_e32 v2, v210
	s_mov_b32 m0, s26
	s_nop 0
	global_load_lds_dwordx4 v2, s[2:3]
	s_waitcnt vmcnt(8)
	s_waitcnt lgkmcnt(0)
	s_barrier
	s_waitcnt lgkmcnt(0)
	v_mfma_scale_f32_16x16x128_f8f6f4 v[112:115], v[20:27], v[180:187], v[112:115], v202, v203 op_sel_hi:[0,0,0]
	v_mfma_scale_f32_16x16x128_f8f6f4 v[108:111], v[28:35], v[180:187], v[108:111], v202, v203 op_sel_hi:[0,0,0]
	v_mfma_scale_f32_16x16x128_f8f6f4 v[104:107], v[20:27], v[188:195], v[104:107], v202, v203 op_sel_hi:[0,0,0]
	v_mfma_scale_f32_16x16x128_f8f6f4 v[100:103], v[28:35], v[188:195], v[100:103], v202, v203 op_sel_hi:[0,0,0]
	v_mfma_scale_f32_16x16x128_f8f6f4 v[96:99], v[20:27], v[230:237], v[96:99], v202, v203 op_sel_hi:[0,0,0]
	v_mfma_scale_f32_16x16x128_f8f6f4 v[92:95], v[28:35], v[230:237], v[92:95], v202, v203 op_sel_hi:[0,0,0]
	v_mfma_scale_f32_16x16x128_f8f6f4 v[88:91], v[20:27], v[238:245], v[88:91], v202, v203 op_sel_hi:[0,0,0]
	v_mfma_scale_f32_16x16x128_f8f6f4 v[84:87], v[28:35], v[238:245], v[84:87], v202, v203 op_sel_hi:[0,0,0]
	v_mfma_scale_f32_16x16x128_f8f6f4 v[80:83], v[4:11], v[180:187], v[80:83], v202, v203 op_sel_hi:[0,0,0]
	v_mfma_scale_f32_16x16x128_f8f6f4 v[76:79], v[12:19], v[180:187], v[76:79], v202, v203 op_sel_hi:[0,0,0]
	v_mfma_scale_f32_16x16x128_f8f6f4 v[72:75], v[4:11], v[188:195], v[72:75], v202, v203 op_sel_hi:[0,0,0]
	v_mfma_scale_f32_16x16x128_f8f6f4 v[68:71], v[12:19], v[188:195], v[68:71], v202, v203 op_sel_hi:[0,0,0]
	v_mfma_scale_f32_16x16x128_f8f6f4 v[64:67], v[4:11], v[230:237], v[64:67], v202, v203 op_sel_hi:[0,0,0]
	v_mfma_scale_f32_16x16x128_f8f6f4 v[60:63], v[12:19], v[230:237], v[60:63], v202, v203 op_sel_hi:[0,0,0]
	v_mfma_scale_f32_16x16x128_f8f6f4 v[56:59], v[4:11], v[238:245], v[56:59], v202, v203 op_sel_hi:[0,0,0]
	v_mfma_scale_f32_16x16x128_f8f6f4 v[52:55], v[12:19], v[238:245], v[52:55], v202, v203 op_sel_hi:[0,0,0]
	s_barrier
	s_add_i32 s25, s25, 2
	s_add_u32 s40, s40, 0x100
	s_addc_u32 s41, s41, 0
	s_cmp_gt_u32 s25, 5
	s_cbranch_scc1 .LBB0_1015

.LBB0_1011:
	ds_read_b128 v[20:23], v222
	ds_read_b128 v[24:27], v222 offset:1024
	ds_read_b128 v[28:31], v222 offset:2048
	ds_read_b128 v[32:35], v222 offset:3072
	ds_read_b128 v[4:7], v223
	ds_read_b128 v[8:11], v223 offset:1024
	ds_read_b128 v[12:15], v223 offset:2048
	ds_read_b128 v[16:19], v223 offset:3072
	v_add_u32_e32 v246, 0xc000, v208
	s_add_u32 s26, s40, 0x80
	v_mov_b32_e32 v2, v211
	v_readfirstlane_b32 s28, v246
	v_add_u32_e32 v246, 0xe000, v208
	ds_read_b128 v[180:183], v226
	ds_read_b128 v[184:187], v226 offset:1024
	ds_read_b128 v[230:233], v227
	ds_read_b128 v[234:237], v227 offset:1024
	ds_read_b128 v[238:241], v228
	ds_read_b128 v[242:245], v228 offset:1024
	ds_read_b128 v[188:191], v229
	ds_read_b128 v[192:195], v229 offset:1024
	s_addc_u32 s27, s41, 0
	s_mov_b32 m0, s28
	v_readfirstlane_b32 s28, v246
	global_load_lds_dwordx4 v2, s[26:27]
	v_mov_b32_e32 v2, v212
	s_mov_b32 m0, s28
	s_nop 0
	global_load_lds_dwordx4 v2, s[26:27]
	s_waitcnt vmcnt(8)
	s_waitcnt lgkmcnt(0)
	s_barrier
	s_waitcnt lgkmcnt(0)
	v_mfma_scale_f32_16x16x128_f8f6f4 v[176:179], v[20:27], v[180:187], v[176:179], v202, v203 op_sel_hi:[0,0,0]
	v_mfma_scale_f32_16x16x128_f8f6f4 v[172:175], v[28:35], v[180:187], v[172:175], v202, v203 op_sel_hi:[0,0,0]
	v_mfma_scale_f32_16x16x128_f8f6f4 v[168:171], v[20:27], v[230:237], v[168:171], v202, v203 op_sel_hi:[0,0,0]
	v_mfma_scale_f32_16x16x128_f8f6f4 v[164:167], v[28:35], v[230:237], v[164:167], v202, v203 op_sel_hi:[0,0,0]
	v_mfma_scale_f32_16x16x128_f8f6f4 v[160:163], v[20:27], v[238:245], v[160:163], v202, v203 op_sel_hi:[0,0,0]
	v_mfma_scale_f32_16x16x128_f8f6f4 v[156:159], v[28:35], v[238:245], v[156:159], v202, v203 op_sel_hi:[0,0,0]
	v_mfma_scale_f32_16x16x128_f8f6f4 v[152:155], v[20:27], v[188:195], v[152:155], v202, v203 op_sel_hi:[0,0,0]
	v_mfma_scale_f32_16x16x128_f8f6f4 v[148:151], v[28:35], v[188:195], v[148:151], v202, v203 op_sel_hi:[0,0,0]
	v_mfma_scale_f32_16x16x128_f8f6f4 v[144:147], v[4:11], v[180:187], v[144:147], v202, v203 op_sel_hi:[0,0,0]
	v_mfma_scale_f32_16x16x128_f8f6f4 v[140:143], v[12:19], v[180:187], v[140:143], v202, v203 op_sel_hi:[0,0,0]
	v_mfma_scale_f32_16x16x128_f8f6f4 v[136:139], v[4:11], v[230:237], v[136:139], v202, v203 op_sel_hi:[0,0,0]
	v_mfma_scale_f32_16x16x128_f8f6f4 v[132:135], v[12:19], v[230:237], v[132:135], v202, v203 op_sel_hi:[0,0,0]
	v_mfma_scale_f32_16x16x128_f8f6f4 v[128:131], v[4:11], v[238:245], v[128:131], v202, v203 op_sel_hi:[0,0,0]
	v_mfma_scale_f32_16x16x128_f8f6f4 v[124:127], v[12:19], v[238:245], v[124:127], v202, v203 op_sel_hi:[0,0,0]
	v_mfma_scale_f32_16x16x128_f8f6f4 v[120:123], v[4:11], v[188:195], v[120:123], v202, v203 op_sel_hi:[0,0,0]
	v_mfma_scale_f32_16x16x128_f8f6f4 v[116:119], v[12:19], v[188:195], v[116:119], v202, v203 op_sel_hi:[0,0,0]
	s_barrier
	s_andn2_b64 vcc, exec, s[2:3]
	s_cbranch_vccnz .LBB0_1014
	s_cmpk_gt_u32 s19, 0x1ff
	s_mov_b64 s[20:21], 0
	s_cbranch_scc1 .LBB0_1007
	v_mov_b32_e32 v2, v0
	s_lshr_b32 s3, s19, 3
	v_ashrrev_i32_e32 v181, 31, v2
	v_lshrrev_b32_e32 v181, 26, v181
	v_lshlrev_b32_e32 v180, 4, v2
	v_add_u32_e32 v181, v2, v181
	v_bfe_i32 v2, v2, 27, 1
	v_lshrrev_b32_e32 v2, 22, v2
	v_add_u32_e32 v2, v180, v2
	v_and_b32_e32 v2, 0xfffffc00, v2
	v_sub_u32_e32 v2, v180, v2
	v_lshrrev_b32_e32 v180, 4, v2
	s_add_i32 s6, s18, s19
	s_and_b32 s2, s19, 7
	s_sub_i32 s10, s3, 32
	v_bitop3_b32 v2, v180, v2, 32 bitop3:0x6c
	s_cmpk_lt_u32 s19, 0x100
	v_ashrrev_i32_e32 v182, 31, v2
	s_cselect_b32 s3, s3, s10
	s_lshr_b32 s10, s19, 5
	v_lshrrev_b32_e32 v182, 26, v182
	s_and_b32 s10, s10, 8
	s_and_b32 s11, s3, 7
	v_add_u32_e32 v182, v2, v182
	s_or_b32 s10, s11, s10
	v_lshrrev_b32_e32 v183, 6, v182
	v_and_b32_e32 v182, 0xc0, v182
	s_lshr_b32 s82, s3, 3
	s_lshl_b32 s3, s10, 3
	v_ashrrev_i32_e32 v181, 6, v181
	v_sub_u32_e32 v2, v2, v182
	s_or_b32 s16, s3, s2
	v_lshlrev_b32_e32 v180, 3, v181
	v_lshlrev_b32_e32 v181, 5, v181
	v_ashrrev_i16_sdwa v2, v196, sext(v2) dst_sel:DWORD dst_unused:UNUSED_PAD src0_sel:DWORD src1_sel:BYTE_0
	s_lshl_b64 s[2:3], s[82:83], 18
	v_and_b32_e32 v180, 0x3ffff0, v180
	v_and_b32_e32 v181, 32, v181
	v_bfe_i32 v2, v2, 0, 16
	s_add_u32 s10, s7, s2
	s_addc_u32 s11, s17, s3
	s_lshl_b32 s2, s16, 18
	v_add_lshl_u32 v180, v183, v180, 10
	v_add_lshl_u32 v2, v181, v2, 1
	v_add3_u32 v209, v180, s2, v2
	v_add_u32_e32 v210, 0x10000, v209
	v_add_u32_e32 v211, 0x20000, v209
	v_add_u32_e32 v212, 0x30000, v209
	s_mov_b64 s[20:21], -1
	s_mov_b32 s19, s6
	s_mov_b32 s6, s82
	s_branch .LBB0_1007

.LBB0_1248:
	ds_read_b128 v[20:23], v212
	ds_read_b128 v[24:27], v212 offset:1024
	ds_read_b128 v[28:31], v212 offset:2048
	ds_read_b128 v[32:35], v212 offset:3072
	ds_read_b128 v[4:7], v213
	ds_read_b128 v[8:11], v213 offset:1024
	ds_read_b128 v[12:15], v213 offset:2048
	ds_read_b128 v[16:19], v213 offset:3072
	s_lshl_b32 s2, s30, 7
	s_add_u32 s2, s6, s2
	s_addc_u32 s3, s7, 0
	v_add_u32_e32 v181, 0xc000, v202
	s_add_u32 s2, s2, 0x80
	v_mov_b32_e32 v2, v185
	v_readfirstlane_b32 s31, v181
	v_add_u32_e32 v181, 0xe000, v202
	ds_read_b128 v[220:223], v216
	ds_read_b128 v[224:227], v216 offset:1024
	ds_read_b128 v[228:231], v217
	ds_read_b128 v[232:235], v217 offset:1024
	ds_read_b128 v[236:239], v218
	ds_read_b128 v[240:243], v218 offset:1024
	ds_read_b128 v[244:247], v219
	ds_read_b128 v[248:251], v219 offset:1024
	s_addc_u32 s3, s3, 0
	s_mov_b32 m0, s31
	v_readfirstlane_b32 s31, v181
	global_load_lds_dwordx4 v2, s[2:3]
	v_mov_b32_e32 v2, v186
	s_mov_b32 m0, s31
	s_nop 0
	global_load_lds_dwordx4 v2, s[2:3]
	s_waitcnt vmcnt(8)
	s_waitcnt lgkmcnt(0)
	s_barrier
	s_waitcnt lgkmcnt(0)
	v_mfma_scale_f32_16x16x128_f8f6f4 v[176:179], v[20:27], v[220:227], v[176:179], v188, v187 op_sel_hi:[0,0,0]
	v_mfma_scale_f32_16x16x128_f8f6f4 v[168:171], v[28:35], v[220:227], v[168:171], v188, v187 op_sel_hi:[0,0,0]
	v_mfma_scale_f32_16x16x128_f8f6f4 v[160:163], v[20:27], v[228:235], v[160:163], v188, v187 op_sel_hi:[0,0,0]
	v_mfma_scale_f32_16x16x128_f8f6f4 v[152:155], v[28:35], v[228:235], v[152:155], v188, v187 op_sel_hi:[0,0,0]
	v_mfma_scale_f32_16x16x128_f8f6f4 v[144:147], v[20:27], v[236:243], v[144:147], v188, v187 op_sel_hi:[0,0,0]
	v_mfma_scale_f32_16x16x128_f8f6f4 v[136:139], v[28:35], v[236:243], v[136:139], v188, v187 op_sel_hi:[0,0,0]
	v_mfma_scale_f32_16x16x128_f8f6f4 v[128:131], v[20:27], v[244:251], v[128:131], v188, v187 op_sel_hi:[0,0,0]
	v_mfma_scale_f32_16x16x128_f8f6f4 v[120:123], v[28:35], v[244:251], v[120:123], v188, v187 op_sel_hi:[0,0,0]
	s_add_i32 s31, s30, 2
	v_mfma_scale_f32_16x16x128_f8f6f4 v[172:175], v[4:11], v[220:227], v[172:175], v188, v187 op_sel_hi:[0,0,0]
	v_mfma_scale_f32_16x16x128_f8f6f4 v[164:167], v[12:19], v[220:227], v[164:167], v188, v187 op_sel_hi:[0,0,0]
	v_mfma_scale_f32_16x16x128_f8f6f4 v[156:159], v[4:11], v[228:235], v[156:159], v188, v187 op_sel_hi:[0,0,0]
	v_mfma_scale_f32_16x16x128_f8f6f4 v[148:151], v[12:19], v[228:235], v[148:151], v188, v187 op_sel_hi:[0,0,0]
	v_mfma_scale_f32_16x16x128_f8f6f4 v[140:143], v[4:11], v[236:243], v[140:143], v188, v187 op_sel_hi:[0,0,0]
	v_mfma_scale_f32_16x16x128_f8f6f4 v[132:135], v[12:19], v[236:243], v[132:135], v188, v187 op_sel_hi:[0,0,0]
	v_mfma_scale_f32_16x16x128_f8f6f4 v[124:127], v[4:11], v[244:251], v[124:127], v188, v187 op_sel_hi:[0,0,0]
	v_mfma_scale_f32_16x16x128_f8f6f4 v[116:119], v[12:19], v[244:251], v[116:119], v188, v187 op_sel_hi:[0,0,0]
	s_cmp_lg_u32 s30, 6
	s_barrier
	s_cbranch_scc1 .LBB0_1253
	s_mov_b64 s[2:3], -1
	s_cmp_ge_u32 s18, s16
	s_mov_b64 s[12:13], -1
	s_cbranch_scc1 .LBB0_1251

.LBB0_1259:
	s_lshl_b64 s[2:3], s[82:83], 7
	s_add_u32 s34, s4, s2
	v_mov_b32_e32 v2, v184
	v_readfirstlane_b32 s33, v189
	ds_read_b128 v[220:223], v216 offset:16384
	ds_read_b128 v[224:227], v216 offset:17408
	ds_read_b128 v[228:231], v217 offset:16384
	ds_read_b128 v[232:235], v217 offset:17408
	ds_read_b128 v[236:239], v218 offset:16384
	ds_read_b128 v[240:243], v218 offset:17408
	ds_read_b128 v[244:247], v219 offset:16384
	ds_read_b128 v[248:251], v219 offset:17408
	s_addc_u32 s35, s5, s3
	s_mov_b32 m0, s33
	s_add_u32 s40, s34, 0x10000
	global_load_lds_dwordx4 v2, s[34:35]
	v_mov_b32_e32 v2, v184
	v_readfirstlane_b32 s33, v190
	s_addc_u32 s41, s35, 0
	s_mov_b32 m0, s33
	v_readfirstlane_b32 s33, v191
	global_load_lds_dwordx4 v2, s[40:41]
	s_add_u32 s40, s34, 0x20000
	v_mov_b32_e32 v2, v184
	s_addc_u32 s41, s35, 0
	s_mov_b32 m0, s33
	s_add_u32 s34, s34, 0x30000
	global_load_lds_dwordx4 v2, s[40:41]
	v_mov_b32_e32 v2, v184
	v_readfirstlane_b32 s33, v201
	s_addc_u32 s35, s35, 0
	s_mov_b32 m0, s33
	s_add_u32 s2, s6, s2
	global_load_lds_dwordx4 v2, s[34:35]
	v_mov_b32_e32 v2, v182
	v_readfirstlane_b32 s33, v202
	s_addc_u32 s3, s7, s3
	s_mov_b32 m0, s33
	v_readfirstlane_b32 s33, v203
	global_load_lds_dwordx4 v2, s[2:3]
	v_mov_b32_e32 v2, v183
	s_mov_b32 m0, s33
	s_nop 0
	global_load_lds_dwordx4 v2, s[2:3]
	s_waitcnt vmcnt(8)
	s_waitcnt lgkmcnt(0)
	s_barrier
	s_waitcnt lgkmcnt(0)
	v_mfma_scale_f32_16x16x128_f8f6f4 v[112:115], v[20:27], v[220:227], v[112:115], v188, v187 op_sel_hi:[0,0,0]
	v_mfma_scale_f32_16x16x128_f8f6f4 v[104:107], v[28:35], v[220:227], v[104:107], v188, v187 op_sel_hi:[0,0,0]
	v_mfma_scale_f32_16x16x128_f8f6f4 v[96:99], v[20:27], v[228:235], v[96:99], v188, v187 op_sel_hi:[0,0,0]
	v_mfma_scale_f32_16x16x128_f8f6f4 v[88:91], v[28:35], v[228:235], v[88:91], v188, v187 op_sel_hi:[0,0,0]
	v_mfma_scale_f32_16x16x128_f8f6f4 v[80:83], v[20:27], v[236:243], v[80:83], v188, v187 op_sel_hi:[0,0,0]
	v_mfma_scale_f32_16x16x128_f8f6f4 v[72:75], v[28:35], v[236:243], v[72:75], v188, v187 op_sel_hi:[0,0,0]
	v_mfma_scale_f32_16x16x128_f8f6f4 v[64:67], v[20:27], v[244:251], v[64:67], v188, v187 op_sel_hi:[0,0,0]
	v_mfma_scale_f32_16x16x128_f8f6f4 v[56:59], v[28:35], v[244:251], v[56:59], v188, v187 op_sel_hi:[0,0,0]
	v_mfma_scale_f32_16x16x128_f8f6f4 v[108:111], v[4:11], v[220:227], v[108:111], v188, v187 op_sel_hi:[0,0,0]
	v_mfma_scale_f32_16x16x128_f8f6f4 v[100:103], v[12:19], v[220:227], v[100:103], v188, v187 op_sel_hi:[0,0,0]
	v_mfma_scale_f32_16x16x128_f8f6f4 v[92:95], v[4:11], v[228:235], v[92:95], v188, v187 op_sel_hi:[0,0,0]
	v_mfma_scale_f32_16x16x128_f8f6f4 v[84:87], v[12:19], v[228:235], v[84:87], v188, v187 op_sel_hi:[0,0,0]
	v_mfma_scale_f32_16x16x128_f8f6f4 v[76:79], v[4:11], v[236:243], v[76:79], v188, v187 op_sel_hi:[0,0,0]
	v_mfma_scale_f32_16x16x128_f8f6f4 v[68:71], v[12:19], v[236:243], v[68:71], v188, v187 op_sel_hi:[0,0,0]
	v_mfma_scale_f32_16x16x128_f8f6f4 v[60:63], v[4:11], v[244:251], v[60:63], v188, v187 op_sel_hi:[0,0,0]
	v_mfma_scale_f32_16x16x128_f8f6f4 v[52:55], v[12:19], v[244:251], v[52:55], v188, v187 op_sel_hi:[0,0,0]
	s_barrier
	ds_read_b128 v[20:23], v214
	ds_read_b128 v[24:27], v214 offset:1024
	ds_read_b128 v[28:31], v214 offset:2048
	ds_read_b128 v[32:35], v214 offset:3072
	ds_read_b128 v[4:7], v215
	ds_read_b128 v[8:11], v215 offset:1024
	ds_read_b128 v[12:15], v215 offset:2048
	ds_read_b128 v[16:19], v215 offset:3072
	v_mov_b32_e32 v2, v185
	v_readfirstlane_b32 s33, v204
	ds_read_b128 v[220:223], v216 offset:32768
	ds_read_b128 v[224:227], v216 offset:33792
	ds_read_b128 v[228:231], v217 offset:32768
	ds_read_b128 v[232:235], v217 offset:33792
	ds_read_b128 v[236:239], v218 offset:32768
	ds_read_b128 v[240:243], v218 offset:33792
	ds_read_b128 v[244:247], v219 offset:32768
	ds_read_b128 v[248:251], v219 offset:33792
	s_mov_b32 m0, s33
	v_readfirstlane_b32 s33, v205
	global_load_lds_dwordx4 v2, s[2:3]
	v_mov_b32_e32 v2, v186
	s_mov_b32 m0, s33
	s_nop 0
	global_load_lds_dwordx4 v2, s[2:3]
	s_waitcnt vmcnt(8)
	s_waitcnt lgkmcnt(0)
	s_barrier
	s_waitcnt lgkmcnt(0)
	v_mfma_scale_f32_16x16x128_f8f6f4 v[176:179], v[20:27], v[220:227], v[176:179], v188, v187 op_sel_hi:[0,0,0]
	v_mfma_scale_f32_16x16x128_f8f6f4 v[168:171], v[28:35], v[220:227], v[168:171], v188, v187 op_sel_hi:[0,0,0]
	v_mfma_scale_f32_16x16x128_f8f6f4 v[160:163], v[20:27], v[228:235], v[160:163], v188, v187 op_sel_hi:[0,0,0]
	v_mfma_scale_f32_16x16x128_f8f6f4 v[152:155], v[28:35], v[228:235], v[152:155], v188, v187 op_sel_hi:[0,0,0]
	v_mfma_scale_f32_16x16x128_f8f6f4 v[144:147], v[20:27], v[236:243], v[144:147], v188, v187 op_sel_hi:[0,0,0]
	v_mfma_scale_f32_16x16x128_f8f6f4 v[136:139], v[28:35], v[236:243], v[136:139], v188, v187 op_sel_hi:[0,0,0]
	v_mfma_scale_f32_16x16x128_f8f6f4 v[128:131], v[20:27], v[244:251], v[128:131], v188, v187 op_sel_hi:[0,0,0]
	v_mfma_scale_f32_16x16x128_f8f6f4 v[120:123], v[28:35], v[244:251], v[120:123], v188, v187 op_sel_hi:[0,0,0]
	v_mfma_scale_f32_16x16x128_f8f6f4 v[172:175], v[4:11], v[220:227], v[172:175], v188, v187 op_sel_hi:[0,0,0]
	v_mfma_scale_f32_16x16x128_f8f6f4 v[164:167], v[12:19], v[220:227], v[164:167], v188, v187 op_sel_hi:[0,0,0]
	v_mfma_scale_f32_16x16x128_f8f6f4 v[156:159], v[4:11], v[228:235], v[156:159], v188, v187 op_sel_hi:[0,0,0]
	v_mfma_scale_f32_16x16x128_f8f6f4 v[148:151], v[12:19], v[228:235], v[148:151], v188, v187 op_sel_hi:[0,0,0]
	v_mfma_scale_f32_16x16x128_f8f6f4 v[140:143], v[4:11], v[236:243], v[140:143], v188, v187 op_sel_hi:[0,0,0]
	v_mfma_scale_f32_16x16x128_f8f6f4 v[132:135], v[12:19], v[236:243], v[132:135], v188, v187 op_sel_hi:[0,0,0]
	v_mfma_scale_f32_16x16x128_f8f6f4 v[124:127], v[4:11], v[244:251], v[124:127], v188, v187 op_sel_hi:[0,0,0]
	v_mfma_scale_f32_16x16x128_f8f6f4 v[116:119], v[12:19], v[244:251], v[116:119], v188, v187 op_sel_hi:[0,0,0]
	s_barrier
	s_add_i32 s82, s82, 1
	s_lshl_b64 s[2:3], s[82:83], 7
	s_add_u32 s34, s4, s2
	v_mov_b32_e32 v2, v184
	v_readfirstlane_b32 s33, v206
	ds_read_b128 v[220:223], v216 offset:49152
	ds_read_b128 v[224:227], v216 offset:50176
	ds_read_b128 v[228:231], v217 offset:49152
	ds_read_b128 v[232:235], v217 offset:50176
	ds_read_b128 v[236:239], v218 offset:49152
	ds_read_b128 v[240:243], v218 offset:50176
	ds_read_b128 v[244:247], v219 offset:49152
	ds_read_b128 v[248:251], v219 offset:50176
	s_addc_u32 s35, s5, s3
	s_mov_b32 m0, s33
	s_add_u32 s40, s34, 0x10000
	global_load_lds_dwordx4 v2, s[34:35]
	v_mov_b32_e32 v2, v184
	v_readfirstlane_b32 s33, v207
	s_addc_u32 s41, s35, 0
	s_mov_b32 m0, s33
	v_readfirstlane_b32 s33, v210
	global_load_lds_dwordx4 v2, s[40:41]
	s_add_u32 s40, s34, 0x20000
	v_mov_b32_e32 v2, v184
	s_addc_u32 s41, s35, 0
	s_mov_b32 m0, s33
	s_add_u32 s34, s34, 0x30000
	global_load_lds_dwordx4 v2, s[40:41]
	v_mov_b32_e32 v2, v184
	v_readfirstlane_b32 s33, v211
	s_addc_u32 s35, s35, 0
	s_mov_b32 m0, s33
	s_add_u32 s2, s6, s2
	global_load_lds_dwordx4 v2, s[34:35]
	v_mov_b32_e32 v2, v182
	v_readfirstlane_b32 s33, v208
	s_addc_u32 s3, s7, s3
	s_mov_b32 m0, s33
	v_readfirstlane_b32 s33, v209
	global_load_lds_dwordx4 v2, s[2:3]
	v_mov_b32_e32 v2, v183
	s_mov_b32 m0, s33
	s_nop 0
	global_load_lds_dwordx4 v2, s[2:3]
	s_waitcnt vmcnt(8)
	s_waitcnt lgkmcnt(0)
	s_barrier
	s_waitcnt lgkmcnt(0)
	v_mfma_scale_f32_16x16x128_f8f6f4 v[112:115], v[20:27], v[220:227], v[112:115], v188, v187 op_sel_hi:[0,0,0]
	v_mfma_scale_f32_16x16x128_f8f6f4 v[104:107], v[28:35], v[220:227], v[104:107], v188, v187 op_sel_hi:[0,0,0]
	v_mfma_scale_f32_16x16x128_f8f6f4 v[96:99], v[20:27], v[228:235], v[96:99], v188, v187 op_sel_hi:[0,0,0]
	v_mfma_scale_f32_16x16x128_f8f6f4 v[88:91], v[28:35], v[228:235], v[88:91], v188, v187 op_sel_hi:[0,0,0]
	v_mfma_scale_f32_16x16x128_f8f6f4 v[80:83], v[20:27], v[236:243], v[80:83], v188, v187 op_sel_hi:[0,0,0]
	v_mfma_scale_f32_16x16x128_f8f6f4 v[72:75], v[28:35], v[236:243], v[72:75], v188, v187 op_sel_hi:[0,0,0]
	v_mfma_scale_f32_16x16x128_f8f6f4 v[64:67], v[20:27], v[244:251], v[64:67], v188, v187 op_sel_hi:[0,0,0]
	v_mfma_scale_f32_16x16x128_f8f6f4 v[56:59], v[28:35], v[244:251], v[56:59], v188, v187 op_sel_hi:[0,0,0]
	v_mfma_scale_f32_16x16x128_f8f6f4 v[108:111], v[4:11], v[220:227], v[108:111], v188, v187 op_sel_hi:[0,0,0]
	v_mfma_scale_f32_16x16x128_f8f6f4 v[100:103], v[12:19], v[220:227], v[100:103], v188, v187 op_sel_hi:[0,0,0]
	v_mfma_scale_f32_16x16x128_f8f6f4 v[92:95], v[4:11], v[228:235], v[92:95], v188, v187 op_sel_hi:[0,0,0]
	v_mfma_scale_f32_16x16x128_f8f6f4 v[84:87], v[12:19], v[228:235], v[84:87], v188, v187 op_sel_hi:[0,0,0]
	v_mfma_scale_f32_16x16x128_f8f6f4 v[76:79], v[4:11], v[236:243], v[76:79], v188, v187 op_sel_hi:[0,0,0]
	v_mfma_scale_f32_16x16x128_f8f6f4 v[68:71], v[12:19], v[236:243], v[68:71], v188, v187 op_sel_hi:[0,0,0]
	v_mfma_scale_f32_16x16x128_f8f6f4 v[60:63], v[4:11], v[244:251], v[60:63], v188, v187 op_sel_hi:[0,0,0]
	v_mfma_scale_f32_16x16x128_f8f6f4 v[52:55], v[12:19], v[244:251], v[52:55], v188, v187 op_sel_hi:[0,0,0]
	s_barrier
	s_cmp_gt_u32 s30, 5
	s_cbranch_scc1 .LBB0_1261
	s_mov_b32 s30, s31
	s_branch .LBB0_1248

.LBB0_1387:
	ds_read_b128 v[20:23], v212
	ds_read_b128 v[24:27], v212 offset:1024
	ds_read_b128 v[28:31], v212 offset:2048
	ds_read_b128 v[32:35], v212 offset:3072
	ds_read_b128 v[4:7], v213
	ds_read_b128 v[8:11], v213 offset:1024
	ds_read_b128 v[12:15], v213 offset:2048
	ds_read_b128 v[16:19], v213 offset:3072
	s_lshl_b32 s2, s23, 7
	s_add_u32 s2, s4, s2
	s_addc_u32 s3, s5, 0
	v_add_u32_e32 v181, 0xc000, v202
	s_add_u32 s2, s2, 0x80
	v_mov_b32_e32 v2, v184
	v_readfirstlane_b32 s24, v181
	v_add_u32_e32 v181, 0xe000, v202
	ds_read_b128 v[222:225], v216
	ds_read_b128 v[226:229], v216 offset:1024
	ds_read_b128 v[230:233], v217
	ds_read_b128 v[234:237], v217 offset:1024
	ds_read_b128 v[238:241], v218
	ds_read_b128 v[242:245], v218 offset:1024
	ds_read_b128 v[36:39], v219
	ds_read_b128 v[40:43], v219 offset:1024
	s_addc_u32 s3, s3, 0
	s_mov_b32 m0, s24
	v_readfirstlane_b32 s24, v181
	global_load_lds_dwordx4 v2, s[2:3]
	v_mov_b32_e32 v2, v185
	s_mov_b32 m0, s24
	s_nop 0
	global_load_lds_dwordx4 v2, s[2:3]
	s_waitcnt vmcnt(8)
	s_waitcnt lgkmcnt(0)
	s_barrier
	s_waitcnt lgkmcnt(0)
	v_mfma_scale_f32_16x16x128_f8f6f4 v[176:179], v[20:27], v[222:229], v[176:179], v188, v187 op_sel_hi:[0,0,0]
	v_mfma_scale_f32_16x16x128_f8f6f4 v[172:175], v[28:35], v[222:229], v[172:175], v188, v187 op_sel_hi:[0,0,0]
	v_mfma_scale_f32_16x16x128_f8f6f4 v[168:171], v[20:27], v[230:237], v[168:171], v188, v187 op_sel_hi:[0,0,0]
	v_mfma_scale_f32_16x16x128_f8f6f4 v[164:167], v[28:35], v[230:237], v[164:167], v188, v187 op_sel_hi:[0,0,0]
	v_mfma_scale_f32_16x16x128_f8f6f4 v[160:163], v[20:27], v[238:245], v[160:163], v188, v187 op_sel_hi:[0,0,0]
	v_mfma_scale_f32_16x16x128_f8f6f4 v[156:159], v[28:35], v[238:245], v[156:159], v188, v187 op_sel_hi:[0,0,0]
	v_mfma_scale_f32_16x16x128_f8f6f4 v[152:155], v[20:27], v[36:43], v[152:155], v188, v187 op_sel_hi:[0,0,0]
	v_mfma_scale_f32_16x16x128_f8f6f4 v[148:151], v[28:35], v[36:43], v[148:151], v188, v187 op_sel_hi:[0,0,0]
	s_add_i32 s24, s23, 2
	v_mfma_scale_f32_16x16x128_f8f6f4 v[120:123], v[4:11], v[222:229], v[120:123], v188, v187 op_sel_hi:[0,0,0]
	v_mfma_scale_f32_16x16x128_f8f6f4 v[116:119], v[12:19], v[222:229], v[116:119], v188, v187 op_sel_hi:[0,0,0]
	v_mfma_scale_f32_16x16x128_f8f6f4 v[112:115], v[4:11], v[230:237], v[112:115], v188, v187 op_sel_hi:[0,0,0]
	v_mfma_scale_f32_16x16x128_f8f6f4 v[108:111], v[12:19], v[230:237], v[108:111], v188, v187 op_sel_hi:[0,0,0]
	v_mfma_scale_f32_16x16x128_f8f6f4 v[96:99], v[4:11], v[238:245], v[96:99], v188, v187 op_sel_hi:[0,0,0]
	v_mfma_scale_f32_16x16x128_f8f6f4 v[92:95], v[12:19], v[238:245], v[92:95], v188, v187 op_sel_hi:[0,0,0]
	v_mfma_scale_f32_16x16x128_f8f6f4 v[88:91], v[4:11], v[36:43], v[88:91], v188, v187 op_sel_hi:[0,0,0]
	v_mfma_scale_f32_16x16x128_f8f6f4 v[84:87], v[12:19], v[36:43], v[84:87], v188, v187 op_sel_hi:[0,0,0]
	s_cmp_lg_u32 s23, 6
	s_barrier
	s_cbranch_scc1 .LBB0_1392
	s_mov_b64 s[2:3], -1
	s_cmp_ge_u32 s14, s13
	s_mov_b64 s[10:11], -1
	s_cbranch_scc1 .LBB0_1390

.LBB0_1398:
	s_lshl_b64 s[2:3], s[82:83], 7
	s_add_u32 s26, s6, s2
	v_mov_b32_e32 v2, v186
	v_readfirstlane_b32 s25, v189
	ds_read_b128 v[36:39], v216 offset:16384
	ds_read_b128 v[40:43], v216 offset:17408
	ds_read_b128 v[222:225], v217 offset:16384
	ds_read_b128 v[226:229], v217 offset:17408
	ds_read_b128 v[230:233], v218 offset:16384
	ds_read_b128 v[234:237], v218 offset:17408
	ds_read_b128 v[238:241], v219 offset:16384
	ds_read_b128 v[242:245], v219 offset:17408
	s_addc_u32 s27, s7, s3
	s_mov_b32 m0, s25
	s_add_u32 s28, s26, 0x10000
	global_load_lds_dwordx4 v2, s[26:27]
	v_mov_b32_e32 v2, v186
	v_readfirstlane_b32 s25, v190
	s_addc_u32 s29, s27, 0
	s_mov_b32 m0, s25
	v_readfirstlane_b32 s25, v191
	global_load_lds_dwordx4 v2, s[28:29]
	s_add_u32 s28, s26, 0x20000
	v_mov_b32_e32 v2, v186
	s_addc_u32 s29, s27, 0
	s_mov_b32 m0, s25
	s_add_u32 s26, s26, 0x30000
	global_load_lds_dwordx4 v2, s[28:29]
	v_mov_b32_e32 v2, v186
	v_readfirstlane_b32 s25, v201
	s_addc_u32 s27, s27, 0
	s_mov_b32 m0, s25
	s_add_u32 s2, s4, s2
	global_load_lds_dwordx4 v2, s[26:27]
	v_mov_b32_e32 v2, v182
	v_readfirstlane_b32 s25, v202
	s_addc_u32 s3, s5, s3
	s_mov_b32 m0, s25
	v_readfirstlane_b32 s25, v203
	global_load_lds_dwordx4 v2, s[2:3]
	v_mov_b32_e32 v2, v183
	s_mov_b32 m0, s25
	s_nop 0
	global_load_lds_dwordx4 v2, s[2:3]
	s_waitcnt vmcnt(8)
	s_waitcnt lgkmcnt(0)
	s_barrier
	s_waitcnt lgkmcnt(0)
	v_mfma_scale_f32_16x16x128_f8f6f4 v[144:147], v[20:27], v[36:43], v[144:147], v188, v187 op_sel_hi:[0,0,0]
	v_mfma_scale_f32_16x16x128_f8f6f4 v[140:143], v[28:35], v[36:43], v[140:143], v188, v187 op_sel_hi:[0,0,0]
	v_mfma_scale_f32_16x16x128_f8f6f4 v[136:139], v[20:27], v[222:229], v[136:139], v188, v187 op_sel_hi:[0,0,0]
	v_mfma_scale_f32_16x16x128_f8f6f4 v[132:135], v[28:35], v[222:229], v[132:135], v188, v187 op_sel_hi:[0,0,0]
	v_mfma_scale_f32_16x16x128_f8f6f4 v[128:131], v[20:27], v[230:237], v[128:131], v188, v187 op_sel_hi:[0,0,0]
	v_mfma_scale_f32_16x16x128_f8f6f4 v[124:127], v[28:35], v[230:237], v[124:127], v188, v187 op_sel_hi:[0,0,0]
	v_mfma_scale_f32_16x16x128_f8f6f4 v[100:103], v[20:27], v[238:245], v[100:103], v188, v187 op_sel_hi:[0,0,0]
	v_mfma_scale_f32_16x16x128_f8f6f4 v[104:107], v[28:35], v[238:245], v[104:107], v188, v187 op_sel_hi:[0,0,0]
	v_mfma_scale_f32_16x16x128_f8f6f4 v[80:83], v[4:11], v[36:43], v[80:83], v188, v187 op_sel_hi:[0,0,0]
	v_mfma_scale_f32_16x16x128_f8f6f4 v[76:79], v[12:19], v[36:43], v[76:79], v188, v187 op_sel_hi:[0,0,0]
	v_mfma_scale_f32_16x16x128_f8f6f4 v[72:75], v[4:11], v[222:229], v[72:75], v188, v187 op_sel_hi:[0,0,0]
	v_mfma_scale_f32_16x16x128_f8f6f4 v[68:71], v[12:19], v[222:229], v[68:71], v188, v187 op_sel_hi:[0,0,0]
	v_mfma_scale_f32_16x16x128_f8f6f4 v[64:67], v[4:11], v[230:237], v[64:67], v188, v187 op_sel_hi:[0,0,0]
	v_mfma_scale_f32_16x16x128_f8f6f4 v[60:63], v[12:19], v[230:237], v[60:63], v188, v187 op_sel_hi:[0,0,0]
	v_mfma_scale_f32_16x16x128_f8f6f4 v[52:55], v[4:11], v[238:245], v[52:55], v188, v187 op_sel_hi:[0,0,0]
	v_mfma_scale_f32_16x16x128_f8f6f4 v[56:59], v[12:19], v[238:245], v[56:59], v188, v187 op_sel_hi:[0,0,0]
	s_barrier
	ds_read_b128 v[20:23], v214
	ds_read_b128 v[24:27], v214 offset:1024
	ds_read_b128 v[28:31], v214 offset:2048
	ds_read_b128 v[32:35], v214 offset:3072
	ds_read_b128 v[4:7], v215
	ds_read_b128 v[8:11], v215 offset:1024
	ds_read_b128 v[12:15], v215 offset:2048
	ds_read_b128 v[16:19], v215 offset:3072
	v_mov_b32_e32 v2, v184
	v_readfirstlane_b32 s25, v204
	ds_read_b128 v[36:39], v216 offset:32768
	ds_read_b128 v[40:43], v216 offset:33792
	ds_read_b128 v[222:225], v217 offset:32768
	ds_read_b128 v[226:229], v217 offset:33792
	ds_read_b128 v[230:233], v218 offset:32768
	ds_read_b128 v[234:237], v218 offset:33792
	ds_read_b128 v[238:241], v219 offset:32768
	ds_read_b128 v[242:245], v219 offset:33792
	s_mov_b32 m0, s25
	v_readfirstlane_b32 s25, v205
	global_load_lds_dwordx4 v2, s[2:3]
	v_mov_b32_e32 v2, v185
	s_mov_b32 m0, s25
	s_nop 0
	global_load_lds_dwordx4 v2, s[2:3]
	s_waitcnt vmcnt(8)
	s_waitcnt lgkmcnt(0)
	s_barrier
	s_waitcnt lgkmcnt(0)
	v_mfma_scale_f32_16x16x128_f8f6f4 v[176:179], v[20:27], v[36:43], v[176:179], v188, v187 op_sel_hi:[0,0,0]
	v_mfma_scale_f32_16x16x128_f8f6f4 v[172:175], v[28:35], v[36:43], v[172:175], v188, v187 op_sel_hi:[0,0,0]
	v_mfma_scale_f32_16x16x128_f8f6f4 v[168:171], v[20:27], v[222:229], v[168:171], v188, v187 op_sel_hi:[0,0,0]
	v_mfma_scale_f32_16x16x128_f8f6f4 v[164:167], v[28:35], v[222:229], v[164:167], v188, v187 op_sel_hi:[0,0,0]
	v_mfma_scale_f32_16x16x128_f8f6f4 v[160:163], v[20:27], v[230:237], v[160:163], v188, v187 op_sel_hi:[0,0,0]
	v_mfma_scale_f32_16x16x128_f8f6f4 v[156:159], v[28:35], v[230:237], v[156:159], v188, v187 op_sel_hi:[0,0,0]
	v_mfma_scale_f32_16x16x128_f8f6f4 v[152:155], v[20:27], v[238:245], v[152:155], v188, v187 op_sel_hi:[0,0,0]
	v_mfma_scale_f32_16x16x128_f8f6f4 v[148:151], v[28:35], v[238:245], v[148:151], v188, v187 op_sel_hi:[0,0,0]
	v_mfma_scale_f32_16x16x128_f8f6f4 v[120:123], v[4:11], v[36:43], v[120:123], v188, v187 op_sel_hi:[0,0,0]
	v_mfma_scale_f32_16x16x128_f8f6f4 v[116:119], v[12:19], v[36:43], v[116:119], v188, v187 op_sel_hi:[0,0,0]
	v_mfma_scale_f32_16x16x128_f8f6f4 v[112:115], v[4:11], v[222:229], v[112:115], v188, v187 op_sel_hi:[0,0,0]
	v_mfma_scale_f32_16x16x128_f8f6f4 v[108:111], v[12:19], v[222:229], v[108:111], v188, v187 op_sel_hi:[0,0,0]
	v_mfma_scale_f32_16x16x128_f8f6f4 v[96:99], v[4:11], v[230:237], v[96:99], v188, v187 op_sel_hi:[0,0,0]
	v_mfma_scale_f32_16x16x128_f8f6f4 v[92:95], v[12:19], v[230:237], v[92:95], v188, v187 op_sel_hi:[0,0,0]
	v_mfma_scale_f32_16x16x128_f8f6f4 v[88:91], v[4:11], v[238:245], v[88:91], v188, v187 op_sel_hi:[0,0,0]
	v_mfma_scale_f32_16x16x128_f8f6f4 v[84:87], v[12:19], v[238:245], v[84:87], v188, v187 op_sel_hi:[0,0,0]
	s_barrier
	s_add_i32 s82, s82, 1
	s_lshl_b64 s[2:3], s[82:83], 7
	s_add_u32 s26, s6, s2
	v_mov_b32_e32 v2, v186
	v_readfirstlane_b32 s25, v206
	ds_read_b128 v[36:39], v216 offset:49152
	ds_read_b128 v[40:43], v216 offset:50176
	ds_read_b128 v[222:225], v217 offset:49152
	ds_read_b128 v[226:229], v217 offset:50176
	ds_read_b128 v[230:233], v218 offset:49152
	ds_read_b128 v[234:237], v218 offset:50176
	ds_read_b128 v[238:241], v219 offset:49152
	ds_read_b128 v[242:245], v219 offset:50176
	s_addc_u32 s27, s7, s3
	s_mov_b32 m0, s25
	s_add_u32 s28, s26, 0x10000
	global_load_lds_dwordx4 v2, s[26:27]
	v_mov_b32_e32 v2, v186
	v_readfirstlane_b32 s25, v207
	s_addc_u32 s29, s27, 0
	s_mov_b32 m0, s25
	v_readfirstlane_b32 s25, v210
	global_load_lds_dwordx4 v2, s[28:29]
	s_add_u32 s28, s26, 0x20000
	v_mov_b32_e32 v2, v186
	s_addc_u32 s29, s27, 0
	s_mov_b32 m0, s25
	s_add_u32 s26, s26, 0x30000
	global_load_lds_dwordx4 v2, s[28:29]
	v_mov_b32_e32 v2, v186
	v_readfirstlane_b32 s25, v211
	s_addc_u32 s27, s27, 0
	s_mov_b32 m0, s25
	s_add_u32 s2, s4, s2
	global_load_lds_dwordx4 v2, s[26:27]
	v_mov_b32_e32 v2, v182
	v_readfirstlane_b32 s25, v208
	s_addc_u32 s3, s5, s3
	s_mov_b32 m0, s25
	v_readfirstlane_b32 s25, v209
	global_load_lds_dwordx4 v2, s[2:3]
	v_mov_b32_e32 v2, v183
	s_mov_b32 m0, s25
	s_nop 0
	global_load_lds_dwordx4 v2, s[2:3]
	s_waitcnt vmcnt(8)
	s_waitcnt lgkmcnt(0)
	s_barrier
	s_waitcnt lgkmcnt(0)
	v_mfma_scale_f32_16x16x128_f8f6f4 v[144:147], v[20:27], v[36:43], v[144:147], v188, v187 op_sel_hi:[0,0,0]
	v_mfma_scale_f32_16x16x128_f8f6f4 v[140:143], v[28:35], v[36:43], v[140:143], v188, v187 op_sel_hi:[0,0,0]
	v_mfma_scale_f32_16x16x128_f8f6f4 v[136:139], v[20:27], v[222:229], v[136:139], v188, v187 op_sel_hi:[0,0,0]
	v_mfma_scale_f32_16x16x128_f8f6f4 v[132:135], v[28:35], v[222:229], v[132:135], v188, v187 op_sel_hi:[0,0,0]
	v_mfma_scale_f32_16x16x128_f8f6f4 v[128:131], v[20:27], v[230:237], v[128:131], v188, v187 op_sel_hi:[0,0,0]
	v_mfma_scale_f32_16x16x128_f8f6f4 v[124:127], v[28:35], v[230:237], v[124:127], v188, v187 op_sel_hi:[0,0,0]
	v_mfma_scale_f32_16x16x128_f8f6f4 v[100:103], v[20:27], v[238:245], v[100:103], v188, v187 op_sel_hi:[0,0,0]
	v_mfma_scale_f32_16x16x128_f8f6f4 v[104:107], v[28:35], v[238:245], v[104:107], v188, v187 op_sel_hi:[0,0,0]
	v_mfma_scale_f32_16x16x128_f8f6f4 v[80:83], v[4:11], v[36:43], v[80:83], v188, v187 op_sel_hi:[0,0,0]
	v_mfma_scale_f32_16x16x128_f8f6f4 v[76:79], v[12:19], v[36:43], v[76:79], v188, v187 op_sel_hi:[0,0,0]
	v_mfma_scale_f32_16x16x128_f8f6f4 v[72:75], v[4:11], v[222:229], v[72:75], v188, v187 op_sel_hi:[0,0,0]
	v_mfma_scale_f32_16x16x128_f8f6f4 v[68:71], v[12:19], v[222:229], v[68:71], v188, v187 op_sel_hi:[0,0,0]
	v_mfma_scale_f32_16x16x128_f8f6f4 v[64:67], v[4:11], v[230:237], v[64:67], v188, v187 op_sel_hi:[0,0,0]
	v_mfma_scale_f32_16x16x128_f8f6f4 v[60:63], v[12:19], v[230:237], v[60:63], v188, v187 op_sel_hi:[0,0,0]
	v_mfma_scale_f32_16x16x128_f8f6f4 v[52:55], v[4:11], v[238:245], v[52:55], v188, v187 op_sel_hi:[0,0,0]
	v_mfma_scale_f32_16x16x128_f8f6f4 v[56:59], v[12:19], v[238:245], v[56:59], v188, v187 op_sel_hi:[0,0,0]
	s_barrier
	s_cmp_gt_u32 s23, 5
	s_cbranch_scc1 .LBB0_1400
	s_mov_b32 s23, s24
	s_branch .LBB0_1387
